# GEMM epilogue stores of the input projection, lora and query phases written through (sc0 sc1): less dirty L2 for the XCD leader to write back at the grid barrier
# baseline (speedup 1.0000x reference)
; __device__ __forceinline__ unsigned cvt_pk_bf16(float lo, float hi) { unsigned r; asm volatile("v_cvt_pk_bf16_f32 %0, %1, %2" : "=v"(r) : "v"(lo), "v"(hi)); return r; }
; __device__ __forceinline__ float fast_sigmoid(float x) { return __builtin_amdgcn_rcpf(1.0f + __builtin_amdgcn_exp2f(-1.44269504089f * x)); }
;     __device__ __forceinline__ void operator()(const f32x4 (&acc)[2][2][4][2], const Unit& u, int wr, int wc, int fr_, int fq_) const {
;     ...
;             for (int m = 0; m < 4; ++m) { bf16_t* rowp = base + (size_t)(row0 + ai * HALF + m * 16) * ldc + col0;
; #pragma unroll
;                 for (int bj = 0; bj < 2; ++bj) { f32x4 v0 = acc[ai][bj][m][0], v1 = acc[ai][bj][m][1];
;                     if (sig) {
; #pragma unroll
;                         for (int j = 0; j < 4; ++j) { v0[j] = fast_sigmoid(v0[j]); v1[j] = fast_sigmoid(v1[j]); } }
;                     u32x4 w; w.x = cvt_pk_bf16(v0[0], v0[1]); w.y = cvt_pk_bf16(v0[2], v0[3]); w.z = cvt_pk_bf16(v1[0], v1[1]); w.w = cvt_pk_bf16(v1[2], v1[3]);
;                     *(u32x4*)(rowp + bj * HALF) = w; } }
;     ...
;             _Pragma("unroll") for (int a_ = 0; a_ < 2; ++a_) _Pragma("unroll") for (int b_ = 0; b_ < 2; ++b_) _Pragma("unroll") for (int m_ = 0; m_ < 4; ++m_) _Pragma("unroll") for (int n_ = 0; n_ < 2; ++n_) { const i32x4 c_ = __builtin_bit_cast(i32x4, acc[a_][b_][m_][n_]);
;                 acc[a_][b_][m_][n_] = (f32x4){(float)c_.x * dq_, (float)c_.y * dq_, (float)c_.z * dq_, (float)c_.w * dq_}; } }
.LBB0_126:
	v_ashrrev_i32_e32 v122, 1, v146
	v_and_b32_e32 v122, -8, v122
	s_add_i32 s61, s61, s93
	v_and_or_b32 v123, v146, 15, s92
	v_add_u32_e32 v122, s61, v122
	v_lshl_add_u32 v150, s74, 8, v123
	v_ashrrev_i32_e32 v123, 31, v122
	v_ashrrev_i32_e32 v124, 31, v150
	v_lshl_add_u64 v[122:123], v[122:123], 1, s[78:79]
	v_mul_lo_u32 v151, s70, v124
	v_mul_lo_u32 v146, s71, v150
	v_mad_u64_u32 v[124:125], s[78:79], s70, v150, 0
	v_add3_u32 v125, v125, v151, v146
	v_cvt_f32_i32_e32 v119, v119
	v_cvt_f32_i32_e32 v118, v118
	v_cvt_f32_i32_e32 v121, v121
	v_cvt_f32_i32_e32 v120, v120
	v_cvt_f32_i32_e32 v115, v115
	v_cvt_f32_i32_e32 v114, v114
	v_cvt_f32_i32_e32 v147, v117
	v_cvt_f32_i32_e32 v146, v116
	v_lshl_add_u64 v[124:125], v[124:125], 1, v[122:123]
	v_pk_mul_f32 v[116:117], v[118:119], s[58:59] op_sel_hi:[1,0]
	v_pk_mul_f32 v[118:119], v[120:121], s[58:59] op_sel_hi:[1,0]
	v_pk_mul_f32 v[120:121], v[114:115], s[58:59] op_sel_hi:[1,0]
	v_pk_mul_f32 v[146:147], v[146:147], s[58:59] op_sel_hi:[1,0]
	s_and_b64 vcc, exec, s[4:5]
	v_cvt_pk_bf16_f32 v126, v126, v127
	v_cvt_pk_bf16_f32 v127, v128, v129
	v_cvt_pk_bf16_f32 v128, v142, v143
	v_cvt_pk_bf16_f32 v129, v144, v145
	global_store_dwordx4 v[124:125], v[126:129], off sc0 sc1
	s_cbranch_vccnz .LBB0_128
	v_mul_f32_e32 v114, 0xbfb8aa3b, v116
	v_exp_f32_e32 v114, v114
	v_mul_f32_e32 v115, 0xbfb8aa3b, v120
	v_exp_f32_e32 v115, v115
	v_add_f32_e32 v114, 1.0, v114
	v_rcp_f32_e32 v116, v114
	v_mul_f32_e32 v114, 0xbfb8aa3b, v117
	v_add_f32_e32 v115, 1.0, v115
	v_exp_f32_e32 v114, v114
	v_mul_f32_e32 v117, 0xbfb8aa3b, v121
	v_exp_f32_e32 v121, v117
	v_rcp_f32_e32 v120, v115
	v_mul_f32_e32 v115, 0xbfb8aa3b, v118
	v_exp_f32_e32 v115, v115
	v_mul_f32_e32 v118, 0xbfb8aa3b, v146
	v_add_f32_e32 v114, 1.0, v114
	v_exp_f32_e32 v126, v118
	v_rcp_f32_e32 v117, v114
	v_add_f32_e32 v114, 1.0, v121
	v_rcp_f32_e32 v121, v114
	v_add_f32_e32 v114, 1.0, v115
	v_mul_f32_e32 v115, 0xbfb8aa3b, v119
	v_exp_f32_e32 v115, v115
	v_mul_f32_e32 v119, 0xbfb8aa3b, v147
	v_rcp_f32_e32 v118, v114
	v_add_f32_e32 v114, 1.0, v126
	v_exp_f32_e32 v126, v119
	v_rcp_f32_e32 v146, v114
	v_add_f32_e32 v114, 1.0, v115
	v_rcp_f32_e32 v119, v114
	v_add_f32_e32 v114, 1.0, v126
	v_rcp_f32_e32 v147, v114
.LBB0_128:
	v_cvt_f32_i32_e32 v111, v111
	v_cvt_f32_i32_e32 v110, v110
	v_cvt_f32_i32_e32 v113, v113
	v_cvt_f32_i32_e32 v112, v112
	v_cvt_f32_i32_e32 v107, v107
	v_cvt_f32_i32_e32 v106, v106
	v_cvt_f32_i32_e32 v115, v109
	v_cvt_f32_i32_e32 v114, v108
	v_pk_mul_f32 v[108:109], v[110:111], s[58:59] op_sel_hi:[1,0]
	v_pk_mul_f32 v[110:111], v[112:113], s[58:59] op_sel_hi:[1,0]
	v_pk_mul_f32 v[112:113], v[106:107], s[58:59] op_sel_hi:[1,0]
	v_pk_mul_f32 v[114:115], v[114:115], s[58:59] op_sel_hi:[1,0]
	s_and_b64 vcc, exec, s[4:5]
	v_cvt_pk_bf16_f32 v116, v116, v117
	v_cvt_pk_bf16_f32 v117, v118, v119
	v_cvt_pk_bf16_f32 v118, v120, v121
	v_cvt_pk_bf16_f32 v119, v146, v147
	global_store_dwordx4 v[124:125], v[116:119], off offset:256 sc0 sc1
	s_cbranch_vccnz .LBB0_130
	v_mul_f32_e32 v106, 0xbfb8aa3b, v108
	v_exp_f32_e32 v106, v106
	v_mul_f32_e32 v107, 0xbfb8aa3b, v112
	v_exp_f32_e32 v107, v107
	v_add_f32_e32 v106, 1.0, v106
	v_rcp_f32_e32 v108, v106
	v_mul_f32_e32 v106, 0xbfb8aa3b, v109
	v_add_f32_e32 v107, 1.0, v107
	v_exp_f32_e32 v106, v106
	v_mul_f32_e32 v109, 0xbfb8aa3b, v113
	v_exp_f32_e32 v113, v109
	v_rcp_f32_e32 v112, v107
	v_mul_f32_e32 v107, 0xbfb8aa3b, v110
	v_exp_f32_e32 v107, v107
	v_add_f32_e32 v106, 1.0, v106
	v_rcp_f32_e32 v109, v106
	v_add_f32_e32 v106, 1.0, v113
	v_mul_f32_e32 v110, 0xbfb8aa3b, v114
	v_exp_f32_e32 v114, v110
	v_rcp_f32_e32 v113, v106
	v_add_f32_e32 v106, 1.0, v107
	v_mul_f32_e32 v107, 0xbfb8aa3b, v111
	v_exp_f32_e32 v107, v107
	v_mul_f32_e32 v111, 0xbfb8aa3b, v115
	v_exp_f32_e32 v115, v111
	v_rcp_f32_e32 v110, v106
	v_add_f32_e32 v106, 1.0, v114
	v_rcp_f32_e32 v114, v106
	v_add_f32_e32 v106, 1.0, v107
	v_rcp_f32_e32 v111, v106
	v_add_f32_e32 v106, 1.0, v115
	v_rcp_f32_e32 v115, v106
.LBB0_130:
	v_or_b32_e32 v106, 16, v150
	v_mul_lo_u32 v116, s71, v106
	v_mad_u64_u32 v[106:107], s[78:79], s70, v106, 0
	v_add3_u32 v107, v107, v151, v116
	v_cvt_f32_i32_e32 v103, v103
	v_cvt_f32_i32_e32 v102, v102
	v_cvt_f32_i32_e32 v105, v105
	v_cvt_f32_i32_e32 v104, v104
	v_cvt_f32_i32_e32 v99, v99
	v_cvt_f32_i32_e32 v98, v98
	v_cvt_f32_i32_e32 v117, v101
	v_cvt_f32_i32_e32 v116, v100
	v_lshl_add_u64 v[106:107], v[106:107], 1, v[122:123]
	v_pk_mul_f32 v[100:101], v[102:103], s[58:59] op_sel_hi:[1,0]
	v_pk_mul_f32 v[102:103], v[104:105], s[58:59] op_sel_hi:[1,0]
	v_pk_mul_f32 v[104:105], v[98:99], s[58:59] op_sel_hi:[1,0]
	v_pk_mul_f32 v[116:117], v[116:117], s[58:59] op_sel_hi:[1,0]
	s_and_b64 vcc, exec, s[4:5]
	v_cvt_pk_bf16_f32 v108, v108, v109
	v_cvt_pk_bf16_f32 v109, v110, v111
	v_cvt_pk_bf16_f32 v110, v112, v113
	v_cvt_pk_bf16_f32 v111, v114, v115
	global_store_dwordx4 v[106:107], v[108:111], off sc0 sc1
	s_cbranch_vccnz .LBB0_132
	v_mul_f32_e32 v98, 0xbfb8aa3b, v100
	v_exp_f32_e32 v98, v98
	v_mul_f32_e32 v99, 0xbfb8aa3b, v104
	v_exp_f32_e32 v99, v99
	v_add_f32_e32 v98, 1.0, v98
	v_rcp_f32_e32 v100, v98
	v_mul_f32_e32 v98, 0xbfb8aa3b, v101
	v_add_f32_e32 v99, 1.0, v99
	v_exp_f32_e32 v98, v98
	v_mul_f32_e32 v101, 0xbfb8aa3b, v105
	v_exp_f32_e32 v105, v101
	v_rcp_f32_e32 v104, v99
	v_mul_f32_e32 v99, 0xbfb8aa3b, v102
	v_exp_f32_e32 v99, v99
	v_mul_f32_e32 v102, 0xbfb8aa3b, v116
	v_add_f32_e32 v98, 1.0, v98
	v_exp_f32_e32 v108, v102
	v_rcp_f32_e32 v101, v98
	v_add_f32_e32 v98, 1.0, v105
	v_rcp_f32_e32 v105, v98
	v_add_f32_e32 v98, 1.0, v99
	v_mul_f32_e32 v99, 0xbfb8aa3b, v103
	v_exp_f32_e32 v99, v99
	v_mul_f32_e32 v103, 0xbfb8aa3b, v117
	v_rcp_f32_e32 v102, v98
	v_add_f32_e32 v98, 1.0, v108
	v_exp_f32_e32 v108, v103
	v_rcp_f32_e32 v116, v98
	v_add_f32_e32 v98, 1.0, v99
	v_rcp_f32_e32 v103, v98
	v_add_f32_e32 v98, 1.0, v108
	v_rcp_f32_e32 v117, v98
; __device__ __forceinline__ unsigned cvt_pk_bf16(float lo, float hi) { unsigned r; asm volatile("v_cvt_pk_bf16_f32 %0, %1, %2" : "=v"(r) : "v"(lo), "v"(hi)); return r; }
; __device__ __forceinline__ float fast_sigmoid(float x) { return __builtin_amdgcn_rcpf(1.0f + __builtin_amdgcn_exp2f(-1.44269504089f * x)); }
;     __device__ __forceinline__ void operator()(const f32x4 (&acc)[2][2][4][2], const Unit& u, int wr, int wc, int fr_, int fq_) const {
;     ...
;             for (int m = 0; m < 4; ++m) { bf16_t* rowp = base + (size_t)(row0 + ai * HALF + m * 16) * ldc + col0;
; #pragma unroll
;                 for (int bj = 0; bj < 2; ++bj) { f32x4 v0 = acc[ai][bj][m][0], v1 = acc[ai][bj][m][1];
;                     if (sig) {
; #pragma unroll
;                         for (int j = 0; j < 4; ++j) { v0[j] = fast_sigmoid(v0[j]); v1[j] = fast_sigmoid(v1[j]); } }
;                     u32x4 w; w.x = cvt_pk_bf16(v0[0], v0[1]); w.y = cvt_pk_bf16(v0[2], v0[3]); w.z = cvt_pk_bf16(v1[0], v1[1]); w.w = cvt_pk_bf16(v1[2], v1[3]);
;                     *(u32x4*)(rowp + bj * HALF) = w; } }
;     ...
;             _Pragma("unroll") for (int a_ = 0; a_ < 2; ++a_) _Pragma("unroll") for (int b_ = 0; b_ < 2; ++b_) _Pragma("unroll") for (int m_ = 0; m_ < 4; ++m_) _Pragma("unroll") for (int n_ = 0; n_ < 2; ++n_) { const i32x4 c_ = __builtin_bit_cast(i32x4, acc[a_][b_][m_][n_]);
;                 acc[a_][b_][m_][n_] = (f32x4){(float)c_.x * dq_, (float)c_.y * dq_, (float)c_.z * dq_, (float)c_.w * dq_}; } }
.LBB0_132:
	v_cvt_f32_i32_e32 v95, v95
	v_cvt_f32_i32_e32 v94, v94
	v_cvt_f32_i32_e32 v97, v97
	v_cvt_f32_i32_e32 v96, v96
	v_cvt_f32_i32_e32 v91, v91
	v_cvt_f32_i32_e32 v90, v90
	v_cvt_f32_i32_e32 v99, v93
	v_cvt_f32_i32_e32 v98, v92
	v_pk_mul_f32 v[92:93], v[94:95], s[58:59] op_sel_hi:[1,0]
	v_pk_mul_f32 v[94:95], v[96:97], s[58:59] op_sel_hi:[1,0]
	v_pk_mul_f32 v[96:97], v[90:91], s[58:59] op_sel_hi:[1,0]
	v_pk_mul_f32 v[98:99], v[98:99], s[58:59] op_sel_hi:[1,0]
	s_and_b64 vcc, exec, s[4:5]
	v_cvt_pk_bf16_f32 v100, v100, v101
	v_cvt_pk_bf16_f32 v101, v102, v103
	v_cvt_pk_bf16_f32 v102, v104, v105
	v_cvt_pk_bf16_f32 v103, v116, v117
	global_store_dwordx4 v[106:107], v[100:103], off offset:256 sc0 sc1
	s_cbranch_vccnz .LBB0_134
	v_mul_f32_e32 v90, 0xbfb8aa3b, v92
	v_exp_f32_e32 v90, v90
	v_mul_f32_e32 v91, 0xbfb8aa3b, v96
	v_exp_f32_e32 v91, v91
	v_add_f32_e32 v90, 1.0, v90
	v_rcp_f32_e32 v92, v90
	v_mul_f32_e32 v90, 0xbfb8aa3b, v93
	v_add_f32_e32 v91, 1.0, v91
	v_exp_f32_e32 v90, v90
	v_mul_f32_e32 v93, 0xbfb8aa3b, v97
	v_exp_f32_e32 v97, v93
	v_rcp_f32_e32 v96, v91
	v_mul_f32_e32 v91, 0xbfb8aa3b, v94
	v_exp_f32_e32 v91, v91
	v_add_f32_e32 v90, 1.0, v90
	v_rcp_f32_e32 v93, v90
	v_add_f32_e32 v90, 1.0, v97
	v_mul_f32_e32 v94, 0xbfb8aa3b, v98
	v_exp_f32_e32 v98, v94
	v_rcp_f32_e32 v97, v90
	v_add_f32_e32 v90, 1.0, v91
	v_mul_f32_e32 v91, 0xbfb8aa3b, v95
	v_exp_f32_e32 v91, v91
	v_mul_f32_e32 v95, 0xbfb8aa3b, v99
	v_exp_f32_e32 v99, v95
	v_rcp_f32_e32 v94, v90
	v_add_f32_e32 v90, 1.0, v98
	v_rcp_f32_e32 v98, v90
	v_add_f32_e32 v90, 1.0, v91
	v_rcp_f32_e32 v95, v90
	v_add_f32_e32 v90, 1.0, v99
	v_rcp_f32_e32 v99, v90
.LBB0_134:
	v_or_b32_e32 v90, 32, v150
	v_mul_lo_u32 v100, s71, v90
	v_mad_u64_u32 v[90:91], s[78:79], s70, v90, 0
	v_add3_u32 v91, v91, v151, v100
	v_cvt_f32_i32_e32 v87, v87
	v_cvt_f32_i32_e32 v86, v86
	v_cvt_f32_i32_e32 v89, v89
	v_cvt_f32_i32_e32 v88, v88
	v_cvt_f32_i32_e32 v83, v83
	v_cvt_f32_i32_e32 v82, v82
	v_cvt_f32_i32_e32 v101, v85
	v_cvt_f32_i32_e32 v100, v84
	v_lshl_add_u64 v[90:91], v[90:91], 1, v[122:123]
	v_pk_mul_f32 v[84:85], v[86:87], s[58:59] op_sel_hi:[1,0]
	v_pk_mul_f32 v[86:87], v[88:89], s[58:59] op_sel_hi:[1,0]
	v_pk_mul_f32 v[88:89], v[82:83], s[58:59] op_sel_hi:[1,0]
	v_pk_mul_f32 v[100:101], v[100:101], s[58:59] op_sel_hi:[1,0]
	s_and_b64 vcc, exec, s[4:5]
	v_cvt_pk_bf16_f32 v92, v92, v93
	v_cvt_pk_bf16_f32 v93, v94, v95
	v_cvt_pk_bf16_f32 v94, v96, v97
	v_cvt_pk_bf16_f32 v95, v98, v99
	global_store_dwordx4 v[90:91], v[92:95], off sc0 sc1
	s_cbranch_vccnz .LBB0_136
	v_mul_f32_e32 v82, 0xbfb8aa3b, v84
	v_exp_f32_e32 v82, v82
	v_mul_f32_e32 v83, 0xbfb8aa3b, v88
	v_exp_f32_e32 v83, v83
	v_add_f32_e32 v82, 1.0, v82
	v_rcp_f32_e32 v84, v82
	v_mul_f32_e32 v82, 0xbfb8aa3b, v85
	v_add_f32_e32 v83, 1.0, v83
	v_exp_f32_e32 v82, v82
	v_mul_f32_e32 v85, 0xbfb8aa3b, v89
	v_exp_f32_e32 v89, v85
	v_rcp_f32_e32 v88, v83
	v_mul_f32_e32 v83, 0xbfb8aa3b, v86
	v_exp_f32_e32 v83, v83
	v_mul_f32_e32 v86, 0xbfb8aa3b, v100
	v_add_f32_e32 v82, 1.0, v82
	v_exp_f32_e32 v92, v86
	v_rcp_f32_e32 v85, v82
	v_add_f32_e32 v82, 1.0, v89
	v_rcp_f32_e32 v89, v82
	v_add_f32_e32 v82, 1.0, v83
	v_mul_f32_e32 v83, 0xbfb8aa3b, v87
	v_exp_f32_e32 v83, v83
	v_mul_f32_e32 v87, 0xbfb8aa3b, v101
	v_rcp_f32_e32 v86, v82
	v_add_f32_e32 v82, 1.0, v92
	v_exp_f32_e32 v92, v87
	v_rcp_f32_e32 v100, v82
	v_add_f32_e32 v82, 1.0, v83
	v_rcp_f32_e32 v87, v82
	v_add_f32_e32 v82, 1.0, v92
	v_rcp_f32_e32 v101, v82
.LBB0_136:
	v_cvt_f32_i32_e32 v79, v79
	v_cvt_f32_i32_e32 v78, v78
	v_cvt_f32_i32_e32 v81, v81
	v_cvt_f32_i32_e32 v80, v80
	v_cvt_f32_i32_e32 v75, v75
	v_cvt_f32_i32_e32 v74, v74
	v_cvt_f32_i32_e32 v83, v77
	v_cvt_f32_i32_e32 v82, v76
	v_pk_mul_f32 v[76:77], v[78:79], s[58:59] op_sel_hi:[1,0]
	v_pk_mul_f32 v[78:79], v[80:81], s[58:59] op_sel_hi:[1,0]
	v_pk_mul_f32 v[80:81], v[74:75], s[58:59] op_sel_hi:[1,0]
	v_pk_mul_f32 v[82:83], v[82:83], s[58:59] op_sel_hi:[1,0]
	s_and_b64 vcc, exec, s[4:5]
	v_cvt_pk_bf16_f32 v84, v84, v85
	v_cvt_pk_bf16_f32 v85, v86, v87
	v_cvt_pk_bf16_f32 v86, v88, v89
	v_cvt_pk_bf16_f32 v87, v100, v101
	global_store_dwordx4 v[90:91], v[84:87], off offset:256 sc0 sc1
	s_cbranch_vccnz .LBB0_138
	v_mul_f32_e32 v74, 0xbfb8aa3b, v76
	v_exp_f32_e32 v74, v74
	v_mul_f32_e32 v75, 0xbfb8aa3b, v80
	v_exp_f32_e32 v75, v75
	v_add_f32_e32 v74, 1.0, v74
	v_rcp_f32_e32 v76, v74
	v_mul_f32_e32 v74, 0xbfb8aa3b, v77
	v_add_f32_e32 v75, 1.0, v75
	v_exp_f32_e32 v74, v74
	v_mul_f32_e32 v77, 0xbfb8aa3b, v81
	v_exp_f32_e32 v81, v77
	v_rcp_f32_e32 v80, v75
	v_mul_f32_e32 v75, 0xbfb8aa3b, v78
	v_exp_f32_e32 v75, v75
	v_add_f32_e32 v74, 1.0, v74
	v_rcp_f32_e32 v77, v74
	v_add_f32_e32 v74, 1.0, v81
	v_mul_f32_e32 v78, 0xbfb8aa3b, v82
	v_exp_f32_e32 v82, v78
	v_rcp_f32_e32 v81, v74
	v_add_f32_e32 v74, 1.0, v75
	v_mul_f32_e32 v75, 0xbfb8aa3b, v79
	v_exp_f32_e32 v75, v75
	v_mul_f32_e32 v79, 0xbfb8aa3b, v83
	v_exp_f32_e32 v83, v79
	v_rcp_f32_e32 v78, v74
	v_add_f32_e32 v74, 1.0, v82
	v_rcp_f32_e32 v82, v74
	v_add_f32_e32 v74, 1.0, v75
	v_rcp_f32_e32 v79, v74
	v_add_f32_e32 v74, 1.0, v83
	v_rcp_f32_e32 v83, v74
; __device__ __forceinline__ unsigned cvt_pk_bf16(float lo, float hi) { unsigned r; asm volatile("v_cvt_pk_bf16_f32 %0, %1, %2" : "=v"(r) : "v"(lo), "v"(hi)); return r; }
; __device__ __forceinline__ float fast_sigmoid(float x) { return __builtin_amdgcn_rcpf(1.0f + __builtin_amdgcn_exp2f(-1.44269504089f * x)); }
;     __device__ __forceinline__ void operator()(const f32x4 (&acc)[2][2][4][2], const Unit& u, int wr, int wc, int fr_, int fq_) const {
;     ...
;             for (int m = 0; m < 4; ++m) { bf16_t* rowp = base + (size_t)(row0 + ai * HALF + m * 16) * ldc + col0;
; #pragma unroll
;                 for (int bj = 0; bj < 2; ++bj) { f32x4 v0 = acc[ai][bj][m][0], v1 = acc[ai][bj][m][1];
;                     if (sig) {
; #pragma unroll
;                         for (int j = 0; j < 4; ++j) { v0[j] = fast_sigmoid(v0[j]); v1[j] = fast_sigmoid(v1[j]); } }
;                     u32x4 w; w.x = cvt_pk_bf16(v0[0], v0[1]); w.y = cvt_pk_bf16(v0[2], v0[3]); w.z = cvt_pk_bf16(v1[0], v1[1]); w.w = cvt_pk_bf16(v1[2], v1[3]);
;                     *(u32x4*)(rowp + bj * HALF) = w; } }
;     ...
;             _Pragma("unroll") for (int a_ = 0; a_ < 2; ++a_) _Pragma("unroll") for (int b_ = 0; b_ < 2; ++b_) _Pragma("unroll") for (int m_ = 0; m_ < 4; ++m_) _Pragma("unroll") for (int n_ = 0; n_ < 2; ++n_) { const i32x4 c_ = __builtin_bit_cast(i32x4, acc[a_][b_][m_][n_]);
;                 acc[a_][b_][m_][n_] = (f32x4){(float)c_.x * dq_, (float)c_.y * dq_, (float)c_.z * dq_, (float)c_.w * dq_}; } }
.LBB0_138:
	v_or_b32_e32 v74, 48, v150
	v_mul_lo_u32 v84, s71, v74
	v_mad_u64_u32 v[74:75], s[78:79], s70, v74, 0
	v_add3_u32 v75, v75, v151, v84
	v_cvt_f32_i32_e32 v71, v71
	v_cvt_f32_i32_e32 v70, v70
	v_cvt_f32_i32_e32 v73, v73
	v_cvt_f32_i32_e32 v72, v72
	v_cvt_f32_i32_e32 v67, v67
	v_cvt_f32_i32_e32 v66, v66
	v_cvt_f32_i32_e32 v85, v69
	v_cvt_f32_i32_e32 v84, v68
	v_lshl_add_u64 v[74:75], v[74:75], 1, v[122:123]
	v_pk_mul_f32 v[68:69], v[70:71], s[58:59] op_sel_hi:[1,0]
	v_pk_mul_f32 v[70:71], v[72:73], s[58:59] op_sel_hi:[1,0]
	v_pk_mul_f32 v[72:73], v[66:67], s[58:59] op_sel_hi:[1,0]
	v_pk_mul_f32 v[84:85], v[84:85], s[58:59] op_sel_hi:[1,0]
	s_and_b64 vcc, exec, s[4:5]
	v_cvt_pk_bf16_f32 v76, v76, v77
	v_cvt_pk_bf16_f32 v77, v78, v79
	v_cvt_pk_bf16_f32 v78, v80, v81
	v_cvt_pk_bf16_f32 v79, v82, v83
	global_store_dwordx4 v[74:75], v[76:79], off sc0 sc1
	s_cbranch_vccnz .LBB0_140
	v_mul_f32_e32 v66, 0xbfb8aa3b, v68
	v_exp_f32_e32 v66, v66
	v_mul_f32_e32 v67, 0xbfb8aa3b, v72
	v_exp_f32_e32 v67, v67
	v_add_f32_e32 v66, 1.0, v66
	v_rcp_f32_e32 v68, v66
	v_mul_f32_e32 v66, 0xbfb8aa3b, v69
	v_add_f32_e32 v67, 1.0, v67
	v_exp_f32_e32 v66, v66
	v_mul_f32_e32 v69, 0xbfb8aa3b, v73
	v_exp_f32_e32 v73, v69
	v_rcp_f32_e32 v72, v67
	v_mul_f32_e32 v67, 0xbfb8aa3b, v70
	v_exp_f32_e32 v67, v67
	v_mul_f32_e32 v70, 0xbfb8aa3b, v84
	v_add_f32_e32 v66, 1.0, v66
	v_exp_f32_e32 v76, v70
	v_rcp_f32_e32 v69, v66
	v_add_f32_e32 v66, 1.0, v73
	v_rcp_f32_e32 v73, v66
	v_add_f32_e32 v66, 1.0, v67
	v_mul_f32_e32 v67, 0xbfb8aa3b, v71
	v_exp_f32_e32 v67, v67
	v_mul_f32_e32 v71, 0xbfb8aa3b, v85
	v_rcp_f32_e32 v70, v66
	v_add_f32_e32 v66, 1.0, v76
	v_exp_f32_e32 v76, v71
	v_rcp_f32_e32 v84, v66
	v_add_f32_e32 v66, 1.0, v67
	v_rcp_f32_e32 v71, v66
	v_add_f32_e32 v66, 1.0, v76
	v_rcp_f32_e32 v85, v66
.LBB0_140:
	v_cvt_f32_i32_e32 v63, v63
	v_cvt_f32_i32_e32 v62, v62
	v_cvt_f32_i32_e32 v65, v65
	v_cvt_f32_i32_e32 v64, v64
	v_cvt_f32_i32_e32 v59, v59
	v_cvt_f32_i32_e32 v58, v58
	v_cvt_f32_i32_e32 v67, v61
	v_cvt_f32_i32_e32 v66, v60
	v_pk_mul_f32 v[60:61], v[62:63], s[58:59] op_sel_hi:[1,0]
	v_pk_mul_f32 v[62:63], v[64:65], s[58:59] op_sel_hi:[1,0]
	v_pk_mul_f32 v[64:65], v[58:59], s[58:59] op_sel_hi:[1,0]
	v_pk_mul_f32 v[66:67], v[66:67], s[58:59] op_sel_hi:[1,0]
	s_and_b64 vcc, exec, s[4:5]
	v_cvt_pk_bf16_f32 v68, v68, v69
	v_cvt_pk_bf16_f32 v69, v70, v71
	v_cvt_pk_bf16_f32 v70, v72, v73
	v_cvt_pk_bf16_f32 v71, v84, v85
	global_store_dwordx4 v[74:75], v[68:71], off offset:256 sc0 sc1
	s_cbranch_vccnz .LBB0_142
	v_mul_f32_e32 v58, 0xbfb8aa3b, v60
	v_exp_f32_e32 v58, v58
	v_mul_f32_e32 v59, 0xbfb8aa3b, v64
	v_exp_f32_e32 v59, v59
	v_add_f32_e32 v58, 1.0, v58
	v_rcp_f32_e32 v60, v58
	v_mul_f32_e32 v58, 0xbfb8aa3b, v61
	v_add_f32_e32 v59, 1.0, v59
	v_exp_f32_e32 v58, v58
	v_mul_f32_e32 v61, 0xbfb8aa3b, v65
	v_exp_f32_e32 v65, v61
	v_rcp_f32_e32 v64, v59
	v_mul_f32_e32 v59, 0xbfb8aa3b, v62
	v_exp_f32_e32 v59, v59
	v_add_f32_e32 v58, 1.0, v58
	v_rcp_f32_e32 v61, v58
	v_add_f32_e32 v58, 1.0, v65
	v_mul_f32_e32 v62, 0xbfb8aa3b, v66
	v_exp_f32_e32 v66, v62
	v_rcp_f32_e32 v65, v58
	v_add_f32_e32 v58, 1.0, v59
	v_mul_f32_e32 v59, 0xbfb8aa3b, v63
	v_exp_f32_e32 v59, v59
	v_mul_f32_e32 v63, 0xbfb8aa3b, v67
	v_exp_f32_e32 v67, v63
	v_rcp_f32_e32 v62, v58
	v_add_f32_e32 v58, 1.0, v66
	v_rcp_f32_e32 v66, v58
	v_add_f32_e32 v58, 1.0, v59
	v_rcp_f32_e32 v63, v58
	v_add_f32_e32 v58, 1.0, v67
	v_rcp_f32_e32 v67, v58
.LBB0_142:
	v_add_u32_e32 v58, 0x80, v150
	v_ashrrev_i32_e32 v59, 31, v58
	v_mul_lo_u32 v68, s70, v59
	v_mul_lo_u32 v69, s71, v58
	v_mad_u64_u32 v[58:59], s[78:79], s70, v58, 0
	v_add3_u32 v59, v59, v68, v69
	v_cvt_f32_i32_e32 v55, v55
	v_cvt_f32_i32_e32 v54, v54
	v_cvt_f32_i32_e32 v57, v57
	v_cvt_f32_i32_e32 v56, v56
	v_cvt_f32_i32_e32 v51, v51
	v_cvt_f32_i32_e32 v50, v50
	v_cvt_f32_i32_e32 v69, v53
	v_cvt_f32_i32_e32 v68, v52
	v_lshl_add_u64 v[58:59], v[58:59], 1, v[122:123]
	v_pk_mul_f32 v[52:53], v[54:55], s[58:59] op_sel_hi:[1,0]
	v_pk_mul_f32 v[54:55], v[56:57], s[58:59] op_sel_hi:[1,0]
	v_pk_mul_f32 v[56:57], v[50:51], s[58:59] op_sel_hi:[1,0]
	v_pk_mul_f32 v[68:69], v[68:69], s[58:59] op_sel_hi:[1,0]
	s_and_b64 vcc, exec, s[4:5]
	v_cvt_pk_bf16_f32 v60, v60, v61
	v_cvt_pk_bf16_f32 v61, v62, v63
	v_cvt_pk_bf16_f32 v62, v64, v65
	v_cvt_pk_bf16_f32 v63, v66, v67
	global_store_dwordx4 v[58:59], v[60:63], off sc0 sc1
	s_cbranch_vccnz .LBB0_144
	v_mul_f32_e32 v50, 0xbfb8aa3b, v52
	v_exp_f32_e32 v50, v50
	v_mul_f32_e32 v51, 0xbfb8aa3b, v56
	v_exp_f32_e32 v51, v51
	v_add_f32_e32 v50, 1.0, v50
	v_rcp_f32_e32 v52, v50
	v_mul_f32_e32 v50, 0xbfb8aa3b, v53
	v_add_f32_e32 v51, 1.0, v51
	v_exp_f32_e32 v50, v50
	v_mul_f32_e32 v53, 0xbfb8aa3b, v57
	v_exp_f32_e32 v57, v53
	v_rcp_f32_e32 v56, v51
	v_mul_f32_e32 v51, 0xbfb8aa3b, v54
	v_exp_f32_e32 v51, v51
	v_mul_f32_e32 v54, 0xbfb8aa3b, v68
	v_add_f32_e32 v50, 1.0, v50
	v_exp_f32_e32 v60, v54
	v_rcp_f32_e32 v53, v50
	v_add_f32_e32 v50, 1.0, v57
	v_rcp_f32_e32 v57, v50
	v_add_f32_e32 v50, 1.0, v51
	v_mul_f32_e32 v51, 0xbfb8aa3b, v55
	v_exp_f32_e32 v51, v51
	v_mul_f32_e32 v55, 0xbfb8aa3b, v69
	v_rcp_f32_e32 v54, v50
	v_add_f32_e32 v50, 1.0, v60
	v_exp_f32_e32 v60, v55
	v_rcp_f32_e32 v68, v50
	v_add_f32_e32 v50, 1.0, v51
	v_rcp_f32_e32 v55, v50
	v_add_f32_e32 v50, 1.0, v60
	v_rcp_f32_e32 v69, v50
; __device__ __forceinline__ unsigned cvt_pk_bf16(float lo, float hi) { unsigned r; asm volatile("v_cvt_pk_bf16_f32 %0, %1, %2" : "=v"(r) : "v"(lo), "v"(hi)); return r; }
; __device__ __forceinline__ float fast_sigmoid(float x) { return __builtin_amdgcn_rcpf(1.0f + __builtin_amdgcn_exp2f(-1.44269504089f * x)); }
;     __device__ __forceinline__ void operator()(const f32x4 (&acc)[2][2][4][2], const Unit& u, int wr, int wc, int fr_, int fq_) const {
;     ...
;             for (int m = 0; m < 4; ++m) { bf16_t* rowp = base + (size_t)(row0 + ai * HALF + m * 16) * ldc + col0;
; #pragma unroll
;                 for (int bj = 0; bj < 2; ++bj) { f32x4 v0 = acc[ai][bj][m][0], v1 = acc[ai][bj][m][1];
;                     if (sig) {
; #pragma unroll
;                         for (int j = 0; j < 4; ++j) { v0[j] = fast_sigmoid(v0[j]); v1[j] = fast_sigmoid(v1[j]); } }
;                     u32x4 w; w.x = cvt_pk_bf16(v0[0], v0[1]); w.y = cvt_pk_bf16(v0[2], v0[3]); w.z = cvt_pk_bf16(v1[0], v1[1]); w.w = cvt_pk_bf16(v1[2], v1[3]);
;                     *(u32x4*)(rowp + bj * HALF) = w; } }
;     ...
;             _Pragma("unroll") for (int a_ = 0; a_ < 2; ++a_) _Pragma("unroll") for (int b_ = 0; b_ < 2; ++b_) _Pragma("unroll") for (int m_ = 0; m_ < 4; ++m_) _Pragma("unroll") for (int n_ = 0; n_ < 2; ++n_) { const i32x4 c_ = __builtin_bit_cast(i32x4, acc[a_][b_][m_][n_]);
;                 acc[a_][b_][m_][n_] = (f32x4){(float)c_.x * dq_, (float)c_.y * dq_, (float)c_.z * dq_, (float)c_.w * dq_}; } }
.LBB0_144:
	v_cvt_f32_i32_e32 v47, v47
	v_cvt_f32_i32_e32 v46, v46
	v_cvt_f32_i32_e32 v49, v49
	v_cvt_f32_i32_e32 v48, v48
	v_cvt_f32_i32_e32 v43, v43
	v_cvt_f32_i32_e32 v42, v42
	v_cvt_f32_i32_e32 v51, v45
	v_cvt_f32_i32_e32 v50, v44
	v_pk_mul_f32 v[44:45], v[46:47], s[58:59] op_sel_hi:[1,0]
	v_pk_mul_f32 v[46:47], v[48:49], s[58:59] op_sel_hi:[1,0]
	v_pk_mul_f32 v[48:49], v[42:43], s[58:59] op_sel_hi:[1,0]
	v_pk_mul_f32 v[50:51], v[50:51], s[58:59] op_sel_hi:[1,0]
	s_and_b64 vcc, exec, s[4:5]
	v_cvt_pk_bf16_f32 v52, v52, v53
	v_cvt_pk_bf16_f32 v53, v54, v55
	v_cvt_pk_bf16_f32 v54, v56, v57
	v_cvt_pk_bf16_f32 v55, v68, v69
	global_store_dwordx4 v[58:59], v[52:55], off offset:256 sc0 sc1
	s_cbranch_vccnz .LBB0_146
	v_mul_f32_e32 v42, 0xbfb8aa3b, v44
	v_exp_f32_e32 v42, v42
	v_mul_f32_e32 v43, 0xbfb8aa3b, v48
	v_exp_f32_e32 v43, v43
	v_add_f32_e32 v42, 1.0, v42
	v_rcp_f32_e32 v44, v42
	v_mul_f32_e32 v42, 0xbfb8aa3b, v45
	v_add_f32_e32 v43, 1.0, v43
	v_exp_f32_e32 v42, v42
	v_mul_f32_e32 v45, 0xbfb8aa3b, v49
	v_exp_f32_e32 v49, v45
	v_rcp_f32_e32 v48, v43
	v_mul_f32_e32 v43, 0xbfb8aa3b, v46
	v_exp_f32_e32 v43, v43
	v_add_f32_e32 v42, 1.0, v42
	v_rcp_f32_e32 v45, v42
	v_add_f32_e32 v42, 1.0, v49
	v_mul_f32_e32 v46, 0xbfb8aa3b, v50
	v_exp_f32_e32 v50, v46
	v_rcp_f32_e32 v49, v42
	v_add_f32_e32 v42, 1.0, v43
	v_mul_f32_e32 v43, 0xbfb8aa3b, v47
	v_exp_f32_e32 v43, v43
	v_mul_f32_e32 v47, 0xbfb8aa3b, v51
	v_exp_f32_e32 v51, v47
	v_rcp_f32_e32 v46, v42
	v_add_f32_e32 v42, 1.0, v50
	v_rcp_f32_e32 v50, v42
	v_add_f32_e32 v42, 1.0, v43
	v_rcp_f32_e32 v47, v42
	v_add_f32_e32 v42, 1.0, v51
	v_rcp_f32_e32 v51, v42
.LBB0_146:
	v_add_u32_e32 v42, 0x90, v150
	v_ashrrev_i32_e32 v43, 31, v42
	v_mul_lo_u32 v52, s70, v43
	v_mul_lo_u32 v53, s71, v42
	v_mad_u64_u32 v[42:43], s[78:79], s70, v42, 0
	v_add3_u32 v43, v43, v52, v53
	v_cvt_f32_i32_e32 v39, v39
	v_cvt_f32_i32_e32 v38, v38
	v_cvt_f32_i32_e32 v41, v41
	v_cvt_f32_i32_e32 v40, v40
	v_cvt_f32_i32_e32 v35, v35
	v_cvt_f32_i32_e32 v34, v34
	v_cvt_f32_i32_e32 v53, v37
	v_cvt_f32_i32_e32 v52, v36
	v_lshl_add_u64 v[42:43], v[42:43], 1, v[122:123]
	v_pk_mul_f32 v[36:37], v[38:39], s[58:59] op_sel_hi:[1,0]
	v_pk_mul_f32 v[38:39], v[40:41], s[58:59] op_sel_hi:[1,0]
	v_pk_mul_f32 v[40:41], v[34:35], s[58:59] op_sel_hi:[1,0]
	v_pk_mul_f32 v[52:53], v[52:53], s[58:59] op_sel_hi:[1,0]
	s_and_b64 vcc, exec, s[4:5]
	v_cvt_pk_bf16_f32 v44, v44, v45
	v_cvt_pk_bf16_f32 v45, v46, v47
	v_cvt_pk_bf16_f32 v46, v48, v49
	v_cvt_pk_bf16_f32 v47, v50, v51
	global_store_dwordx4 v[42:43], v[44:47], off sc0 sc1
	s_cbranch_vccnz .LBB0_148
	v_mul_f32_e32 v34, 0xbfb8aa3b, v36
	v_exp_f32_e32 v34, v34
	v_mul_f32_e32 v35, 0xbfb8aa3b, v40
	v_exp_f32_e32 v35, v35
	v_add_f32_e32 v34, 1.0, v34
	v_rcp_f32_e32 v36, v34
	v_mul_f32_e32 v34, 0xbfb8aa3b, v37
	v_add_f32_e32 v35, 1.0, v35
	v_exp_f32_e32 v34, v34
	v_mul_f32_e32 v37, 0xbfb8aa3b, v41
	v_exp_f32_e32 v41, v37
	v_rcp_f32_e32 v40, v35
	v_mul_f32_e32 v35, 0xbfb8aa3b, v38
	v_exp_f32_e32 v35, v35
	v_mul_f32_e32 v38, 0xbfb8aa3b, v52
	v_add_f32_e32 v34, 1.0, v34
	v_exp_f32_e32 v44, v38
	v_rcp_f32_e32 v37, v34
	v_add_f32_e32 v34, 1.0, v41
	v_rcp_f32_e32 v41, v34
	v_add_f32_e32 v34, 1.0, v35
	v_mul_f32_e32 v35, 0xbfb8aa3b, v39
	v_exp_f32_e32 v35, v35
	v_mul_f32_e32 v39, 0xbfb8aa3b, v53
	v_rcp_f32_e32 v38, v34
	v_add_f32_e32 v34, 1.0, v44
	v_exp_f32_e32 v44, v39
	v_rcp_f32_e32 v52, v34
	v_add_f32_e32 v34, 1.0, v35
	v_rcp_f32_e32 v39, v34
	v_add_f32_e32 v34, 1.0, v44
	v_rcp_f32_e32 v53, v34
.LBB0_148:
	v_cvt_f32_i32_e32 v31, v31
	v_cvt_f32_i32_e32 v30, v30
	v_cvt_f32_i32_e32 v33, v33
	v_cvt_f32_i32_e32 v32, v32
	v_cvt_f32_i32_e32 v27, v27
	v_cvt_f32_i32_e32 v26, v26
	v_cvt_f32_i32_e32 v35, v29
	v_cvt_f32_i32_e32 v34, v28
	v_pk_mul_f32 v[28:29], v[30:31], s[58:59] op_sel_hi:[1,0]
	v_pk_mul_f32 v[30:31], v[32:33], s[58:59] op_sel_hi:[1,0]
	v_pk_mul_f32 v[32:33], v[26:27], s[58:59] op_sel_hi:[1,0]
	v_pk_mul_f32 v[34:35], v[34:35], s[58:59] op_sel_hi:[1,0]
	s_and_b64 vcc, exec, s[4:5]
	v_cvt_pk_bf16_f32 v36, v36, v37
	v_cvt_pk_bf16_f32 v37, v38, v39
	v_cvt_pk_bf16_f32 v38, v40, v41
	v_cvt_pk_bf16_f32 v39, v52, v53
	global_store_dwordx4 v[42:43], v[36:39], off offset:256 sc0 sc1
	s_cbranch_vccnz .LBB0_150
	v_mul_f32_e32 v26, 0xbfb8aa3b, v28
	v_exp_f32_e32 v26, v26
	v_mul_f32_e32 v27, 0xbfb8aa3b, v32
	v_exp_f32_e32 v27, v27
	v_add_f32_e32 v26, 1.0, v26
	v_rcp_f32_e32 v28, v26
	v_mul_f32_e32 v26, 0xbfb8aa3b, v29
	v_add_f32_e32 v27, 1.0, v27
	v_exp_f32_e32 v26, v26
	v_mul_f32_e32 v29, 0xbfb8aa3b, v33
	v_exp_f32_e32 v33, v29
	v_rcp_f32_e32 v32, v27
	v_mul_f32_e32 v27, 0xbfb8aa3b, v30
	v_exp_f32_e32 v27, v27
	v_add_f32_e32 v26, 1.0, v26
	v_rcp_f32_e32 v29, v26
	v_add_f32_e32 v26, 1.0, v33
	v_mul_f32_e32 v30, 0xbfb8aa3b, v34
	v_exp_f32_e32 v34, v30
	v_rcp_f32_e32 v33, v26
	v_add_f32_e32 v26, 1.0, v27
	v_mul_f32_e32 v27, 0xbfb8aa3b, v31
	v_exp_f32_e32 v27, v27
	v_mul_f32_e32 v31, 0xbfb8aa3b, v35
	v_exp_f32_e32 v35, v31
	v_rcp_f32_e32 v30, v26
	v_add_f32_e32 v26, 1.0, v34
	v_rcp_f32_e32 v34, v26
	v_add_f32_e32 v26, 1.0, v27
	v_rcp_f32_e32 v31, v26
	v_add_f32_e32 v26, 1.0, v35
	v_rcp_f32_e32 v35, v26
; __device__ __forceinline__ unsigned cvt_pk_bf16(float lo, float hi) { unsigned r; asm volatile("v_cvt_pk_bf16_f32 %0, %1, %2" : "=v"(r) : "v"(lo), "v"(hi)); return r; }
; __device__ __forceinline__ float fast_sigmoid(float x) { return __builtin_amdgcn_rcpf(1.0f + __builtin_amdgcn_exp2f(-1.44269504089f * x)); }
;     __device__ __forceinline__ void operator()(const f32x4 (&acc)[2][2][4][2], const Unit& u, int wr, int wc, int fr_, int fq_) const {
;     ...
;             for (int m = 0; m < 4; ++m) { bf16_t* rowp = base + (size_t)(row0 + ai * HALF + m * 16) * ldc + col0;
; #pragma unroll
;                 for (int bj = 0; bj < 2; ++bj) { f32x4 v0 = acc[ai][bj][m][0], v1 = acc[ai][bj][m][1];
;                     if (sig) {
; #pragma unroll
;                         for (int j = 0; j < 4; ++j) { v0[j] = fast_sigmoid(v0[j]); v1[j] = fast_sigmoid(v1[j]); } }
;                     u32x4 w; w.x = cvt_pk_bf16(v0[0], v0[1]); w.y = cvt_pk_bf16(v0[2], v0[3]); w.z = cvt_pk_bf16(v1[0], v1[1]); w.w = cvt_pk_bf16(v1[2], v1[3]);
;                     *(u32x4*)(rowp + bj * HALF) = w; } }
;     ...
;             _Pragma("unroll") for (int a_ = 0; a_ < 2; ++a_) _Pragma("unroll") for (int b_ = 0; b_ < 2; ++b_) _Pragma("unroll") for (int m_ = 0; m_ < 4; ++m_) _Pragma("unroll") for (int n_ = 0; n_ < 2; ++n_) { const i32x4 c_ = __builtin_bit_cast(i32x4, acc[a_][b_][m_][n_]);
;                 acc[a_][b_][m_][n_] = (f32x4){(float)c_.x * dq_, (float)c_.y * dq_, (float)c_.z * dq_, (float)c_.w * dq_}; } }
.LBB0_150:
	v_add_u32_e32 v26, 0xa0, v150
	v_ashrrev_i32_e32 v27, 31, v26
	v_mul_lo_u32 v36, s70, v27
	v_mul_lo_u32 v37, s71, v26
	v_mad_u64_u32 v[26:27], s[78:79], s70, v26, 0
	v_add3_u32 v27, v27, v36, v37
	v_cvt_f32_i32_e32 v23, v23
	v_cvt_f32_i32_e32 v22, v22
	v_cvt_f32_i32_e32 v25, v25
	v_cvt_f32_i32_e32 v24, v24
	v_cvt_f32_i32_e32 v37, v19
	v_cvt_f32_i32_e32 v36, v18
	v_cvt_f32_i32_e32 v39, v21
	v_cvt_f32_i32_e32 v38, v20
	v_lshl_add_u64 v[26:27], v[26:27], 1, v[122:123]
	v_pk_mul_f32 v[18:19], v[22:23], s[58:59] op_sel_hi:[1,0]
	v_pk_mul_f32 v[20:21], v[24:25], s[58:59] op_sel_hi:[1,0]
	v_pk_mul_f32 v[22:23], v[36:37], s[58:59] op_sel_hi:[1,0]
	v_pk_mul_f32 v[24:25], v[38:39], s[58:59] op_sel_hi:[1,0]
	s_and_b64 vcc, exec, s[4:5]
	v_cvt_pk_bf16_f32 v28, v28, v29
	v_cvt_pk_bf16_f32 v29, v30, v31
	v_cvt_pk_bf16_f32 v30, v32, v33
	v_cvt_pk_bf16_f32 v31, v34, v35
	global_store_dwordx4 v[26:27], v[28:31], off sc0 sc1
	s_cbranch_vccnz .LBB0_152
	v_mul_f32_e32 v18, 0xbfb8aa3b, v18
	v_mul_f32_e32 v22, 0xbfb8aa3b, v22
	v_mul_f32_e32 v19, 0xbfb8aa3b, v19
	v_mul_f32_e32 v23, 0xbfb8aa3b, v23
	v_mul_f32_e32 v20, 0xbfb8aa3b, v20
	v_mul_f32_e32 v24, 0xbfb8aa3b, v24
	v_mul_f32_e32 v21, 0xbfb8aa3b, v21
	v_mul_f32_e32 v25, 0xbfb8aa3b, v25
	v_exp_f32_e32 v18, v18
	v_exp_f32_e32 v22, v22
	v_exp_f32_e32 v19, v19
	v_exp_f32_e32 v23, v23
	v_exp_f32_e32 v20, v20
	v_exp_f32_e32 v24, v24
	v_exp_f32_e32 v21, v21
	v_exp_f32_e32 v25, v25
	v_add_f32_e32 v18, 1.0, v18
	v_add_f32_e32 v22, 1.0, v22
	v_add_f32_e32 v19, 1.0, v19
	v_add_f32_e32 v23, 1.0, v23
	v_add_f32_e32 v20, 1.0, v20
	v_add_f32_e32 v24, 1.0, v24
	v_add_f32_e32 v21, 1.0, v21
	v_add_f32_e32 v25, 1.0, v25
	v_rcp_f32_e32 v18, v18
	v_rcp_f32_e32 v22, v22
	v_rcp_f32_e32 v19, v19
	v_rcp_f32_e32 v23, v23
	v_rcp_f32_e32 v20, v20
	v_rcp_f32_e32 v24, v24
	v_rcp_f32_e32 v21, v21
	v_rcp_f32_e32 v25, v25
.LBB0_152:
	v_cvt_f32_i32_e32 v15, v15
	v_cvt_f32_i32_e32 v14, v14
	v_cvt_f32_i32_e32 v17, v17
	v_cvt_f32_i32_e32 v16, v16
	v_cvt_f32_i32_e32 v29, v11
	v_cvt_f32_i32_e32 v28, v10
	v_cvt_f32_i32_e32 v31, v13
	v_cvt_f32_i32_e32 v30, v12
	v_pk_mul_f32 v[10:11], v[14:15], s[58:59] op_sel_hi:[1,0]
	v_pk_mul_f32 v[12:13], v[16:17], s[58:59] op_sel_hi:[1,0]
	v_pk_mul_f32 v[14:15], v[28:29], s[58:59] op_sel_hi:[1,0]
	v_pk_mul_f32 v[16:17], v[30:31], s[58:59] op_sel_hi:[1,0]
	s_and_b64 vcc, exec, s[4:5]
	v_cvt_pk_bf16_f32 v18, v18, v19
	v_cvt_pk_bf16_f32 v19, v20, v21
	v_cvt_pk_bf16_f32 v20, v22, v23
	v_cvt_pk_bf16_f32 v21, v24, v25
	global_store_dwordx4 v[26:27], v[18:21], off offset:256 sc0 sc1
	s_cbranch_vccnz .LBB0_154
	v_mul_f32_e32 v10, 0xbfb8aa3b, v10
	v_mul_f32_e32 v14, 0xbfb8aa3b, v14
	v_mul_f32_e32 v11, 0xbfb8aa3b, v11
	v_mul_f32_e32 v15, 0xbfb8aa3b, v15
	v_mul_f32_e32 v12, 0xbfb8aa3b, v12
	v_mul_f32_e32 v16, 0xbfb8aa3b, v16
	v_mul_f32_e32 v13, 0xbfb8aa3b, v13
	v_mul_f32_e32 v17, 0xbfb8aa3b, v17
	v_exp_f32_e32 v10, v10
	v_exp_f32_e32 v14, v14
	v_exp_f32_e32 v11, v11
	v_exp_f32_e32 v15, v15
	v_exp_f32_e32 v12, v12
	v_exp_f32_e32 v16, v16
	v_exp_f32_e32 v13, v13
	v_exp_f32_e32 v17, v17
	v_add_f32_e32 v10, 1.0, v10
	v_add_f32_e32 v14, 1.0, v14
	v_add_f32_e32 v11, 1.0, v11
	v_add_f32_e32 v15, 1.0, v15
	v_add_f32_e32 v12, 1.0, v12
	v_add_f32_e32 v16, 1.0, v16
	v_add_f32_e32 v13, 1.0, v13
	v_add_f32_e32 v17, 1.0, v17
	v_rcp_f32_e32 v10, v10
	v_rcp_f32_e32 v14, v14
	v_rcp_f32_e32 v11, v11
	v_rcp_f32_e32 v15, v15
	v_rcp_f32_e32 v12, v12
	v_rcp_f32_e32 v16, v16
	v_rcp_f32_e32 v13, v13
	v_rcp_f32_e32 v17, v17
.LBB0_154:
	s_nop 0
	v_add_u32_e32 v18, 0xb0, v150
	v_ashrrev_i32_e32 v19, 31, v18
	v_mul_lo_u32 v20, s70, v19
	v_mul_lo_u32 v21, s71, v18
	v_mad_u64_u32 v[18:19], s[70:71], s70, v18, 0
	v_add3_u32 v19, v19, v20, v21
	v_cvt_f32_i32_e32 v7, v7
	v_cvt_f32_i32_e32 v6, v6
	v_cvt_f32_i32_e32 v9, v9
	v_cvt_f32_i32_e32 v8, v8
	v_cvt_f32_i32_e32 v21, v3
	v_cvt_f32_i32_e32 v20, v2
	v_cvt_f32_i32_e32 v23, v5
	v_cvt_f32_i32_e32 v22, v4
	v_lshl_add_u64 v[18:19], v[18:19], 1, v[122:123]
	v_pk_mul_f32 v[2:3], v[6:7], s[58:59] op_sel_hi:[1,0]
	v_pk_mul_f32 v[4:5], v[8:9], s[58:59] op_sel_hi:[1,0]
	v_pk_mul_f32 v[6:7], v[20:21], s[58:59] op_sel_hi:[1,0]
	v_pk_mul_f32 v[8:9], v[22:23], s[58:59] op_sel_hi:[1,0]
	s_and_b64 vcc, exec, s[4:5]
	v_cvt_pk_bf16_f32 v10, v10, v11
	v_cvt_pk_bf16_f32 v11, v12, v13
	v_cvt_pk_bf16_f32 v12, v14, v15
	v_cvt_pk_bf16_f32 v13, v16, v17
	global_store_dwordx4 v[18:19], v[10:13], off sc0 sc1
	s_cbranch_vccnz .LBB0_156
	v_mul_f32_e32 v2, 0xbfb8aa3b, v2
	v_mul_f32_e32 v6, 0xbfb8aa3b, v6
	v_mul_f32_e32 v3, 0xbfb8aa3b, v3
	v_mul_f32_e32 v7, 0xbfb8aa3b, v7
	v_mul_f32_e32 v4, 0xbfb8aa3b, v4
	v_mul_f32_e32 v8, 0xbfb8aa3b, v8
	v_mul_f32_e32 v5, 0xbfb8aa3b, v5
	v_mul_f32_e32 v9, 0xbfb8aa3b, v9
	v_exp_f32_e32 v2, v2
	v_exp_f32_e32 v6, v6
	v_exp_f32_e32 v3, v3
	v_exp_f32_e32 v7, v7
	v_exp_f32_e32 v4, v4
	v_exp_f32_e32 v8, v8
	v_exp_f32_e32 v5, v5
	v_exp_f32_e32 v9, v9
	v_add_f32_e32 v2, 1.0, v2
	v_add_f32_e32 v6, 1.0, v6
	v_add_f32_e32 v3, 1.0, v3
	v_add_f32_e32 v7, 1.0, v7
	v_add_f32_e32 v4, 1.0, v4
	v_add_f32_e32 v8, 1.0, v8
	v_add_f32_e32 v5, 1.0, v5
	v_add_f32_e32 v9, 1.0, v9
	v_rcp_f32_e32 v2, v2
	v_rcp_f32_e32 v6, v6
	v_rcp_f32_e32 v3, v3
	v_rcp_f32_e32 v7, v7
	v_rcp_f32_e32 v4, v4
	v_rcp_f32_e32 v8, v8
	v_rcp_f32_e32 v5, v5
	v_rcp_f32_e32 v9, v9
.LBB0_156:
	s_andn2_b64 vcc, exec, s[0:1]
	s_mov_b64 s[0:1], -1
	v_cvt_pk_bf16_f32 v2, v2, v3
	v_cvt_pk_bf16_f32 v3, v4, v5
	v_cvt_pk_bf16_f32 v4, v6, v7
	v_cvt_pk_bf16_f32 v5, v8, v9
	global_store_dwordx4 v[18:19], v[2:5], off offset:256 sc0 sc1
	s_cbranch_vccnz .LBB0_109
	s_andn2_b64 vcc, exec, s[28:29]
	s_cbranch_vccnz .LBB0_108
	s_barrier
	s_branch .LBB0_108

; __device__ __forceinline__ unsigned cvt_pk_bf16(float lo, float hi) { unsigned r; asm volatile("v_cvt_pk_bf16_f32 %0, %1, %2" : "=v"(r) : "v"(lo), "v"(hi)); return r; }
; __device__ __forceinline__ float fast_sigmoid(float x) { return __builtin_amdgcn_rcpf(1.0f + __builtin_amdgcn_exp2f(-1.44269504089f * x)); }
;     __device__ __forceinline__ void operator()(const f32x4 (&acc)[2][2][4][2], const Unit& u, int wr, int wc, int fr_, int fq_) const {
;     ...
;         const int mode = u.pn >> 3; float* base = WDEC + (size_t)mode * ((size_t)8192 * 2048);
;         bf16_t* baseh = (bf16_t*)base;
;         const int row0 = u.pm * BM + wr * 64 + fr, col0 = (u.pn & 7) * BM + wc * 32 + 8 * fq;
;         const float* bp = mode == 0 ? w0 : a0;
; #pragma unroll
;         for (int ai = 0; ai < 2; ++ai)
; #pragma unroll
;             for (int m = 0; m < 4; ++m) { const size_t ro = (size_t)(row0 + ai * HALF + m * 16) * 2048 + col0;
; #pragma unroll
;                 for (int bj = 0; bj < 2; ++bj) { f32x4 v0 = acc[ai][bj][m][0], v1 = acc[ai][bj][m][1];
;                     if (mode < 2) { v0 += *(const f32x4*)(bp + col0 + bj * HALF); v1 += *(const f32x4*)(bp + col0 + bj * HALF + 4); }
;                     if (mode == 0) {
; #pragma unroll
;                         for (int j = 0; j < 4; ++j) { const float x0 = -v0[j]; const float s0 = fmaxf(x0, 0.f) + __logf(1.0f + __expf(-fabsf(x0))); v0[j] = __expf(-__expf(-s0 - 0.5f));
;                             const float x1 = -v1[j]; const float s1 = fmaxf(x1, 0.f) + __logf(1.0f + __expf(-fabsf(x1))); v1[j] = __expf(-__expf(-s1 - 0.5f)); } }
;                     else if (mode == 1) {
; #pragma unroll
;                         for (int j = 0; j < 4; ++j) { v0[j] = fast_sigmoid(v0[j]); v1[j] = fast_sigmoid(v1[j]); } }
;                     if (mode == 0) { *(f32x4*)(base + ro + bj * HALF) = v0; *(f32x4*)(base + ro + bj * HALF + 4) = v1; }
;                     else { u32x4 w; w.x = cvt_pk_bf16(v0[0], v0[1]); w.y = cvt_pk_bf16(v0[2], v0[3]); w.z = cvt_pk_bf16(v1[0], v1[1]); w.w = cvt_pk_bf16(v1[2], v1[3]); *(u32x4*)(baseh + ro + bj * HALF) = w; } }
.LBB0_1605:
	s_ashr_i32 s9, s8, 31
	s_lshl_b64 s[6:7], s[8:9], 26
	s_add_u32 s90, s95, s6
	s_addc_u32 s91, s96, s7
	s_lshl_b32 s6, s63, 8
	s_add_i32 s6, s6, s75
	v_and_or_b32 v158, v158, 15, s6
	v_ashrrev_i32_e32 v159, 31, v158
	v_lshlrev_b64 v[122:123], 11, v[158:159]
	v_lshl_add_u64 v[122:123], v[122:123], 0, v[156:157]
	v_lshlrev_b64 v[122:123], 1, v[122:123]
	v_lshl_add_u64 v[160:161], s[90:91], 0, v[122:123]
	s_mov_b64 s[6:7], -1
	s_and_b64 vcc, exec, s[10:11]
	s_cbranch_vccz .LBB0_1615
	v_cvt_pk_bf16_f32 v124, v130, v131
	v_cvt_pk_bf16_f32 v125, v132, v133
	v_cvt_pk_bf16_f32 v126, v134, v135
	v_cvt_pk_bf16_f32 v127, v136, v137
	global_store_dwordx4 v[160:161], v[124:127], off sc0 sc1
	v_lshl_add_u64 v[162:163], v[160:161], 0, v[122:123]
	s_cbranch_execz .LBB0_1616

; __device__ __forceinline__ unsigned cvt_pk_bf16(float lo, float hi) { unsigned r; asm volatile("v_cvt_pk_bf16_f32 %0, %1, %2" : "=v"(r) : "v"(lo), "v"(hi)); return r; }
;     __device__ __forceinline__ void operator()(const f32x4 (&acc)[2][2][4][2], const Unit& u, int wr, int wc, int fr_, int fq_) const {
;     ...
;                     else { u32x4 w; w.x = cvt_pk_bf16(v0[0], v0[1]); w.y = cvt_pk_bf16(v0[2], v0[3]); w.z = cvt_pk_bf16(v1[0], v1[1]); w.w = cvt_pk_bf16(v1[2], v1[3]); *(u32x4*)(baseh + ro + bj * HALF) = w; } }
.LBB0_1614:
	v_cvt_pk_bf16_f32 v114, v122, v123
	v_cvt_pk_bf16_f32 v115, v124, v125
	v_cvt_pk_bf16_f32 v116, v126, v127
	v_cvt_pk_bf16_f32 v117, v128, v129
	global_store_dwordx4 v[160:161], v[114:117], off offset:256 sc0 sc1
	s_cbranch_execz .LBB0_1620
	s_branch .LBB0_1621

;     __device__ __forceinline__ void operator()(const f32x4 (&acc)[2][2][4][2], const Unit& u, int wr, int wc, int fr_, int fq_) const {
;     ...
;                     if (mode == 0) { *(f32x4*)(base + ro + bj * HALF) = v0; *(f32x4*)(base + ro + bj * HALF + 4) = v1; }
.LBB0_1616:
	global_store_dwordx4 v[162:163], v[130:133], off sc0 sc1
	global_store_dwordx4 v[162:163], v[134:137], off offset:16 sc0 sc1
	v_cndmask_b32_e64 v122, 0, 1, s[92:93]
	v_cmp_ne_u32_e64 s[8:9], 1, v122
	s_andn2_b64 vcc, exec, s[92:93]
	s_cbranch_vccz .LBB0_1608
	s_branch .LBB0_1609

;     __device__ __forceinline__ void operator()(const f32x4 (&acc)[2][2][4][2], const Unit& u, int wr, int wc, int fr_, int fq_) const {
;     ...
;                     if (mode == 0) { *(f32x4*)(base + ro + bj * HALF) = v0; *(f32x4*)(base + ro + bj * HALF + 4) = v1; }
.LBB0_1620:
	global_store_dwordx4 v[162:163], v[122:125], off offset:512 sc0 sc1
	global_store_dwordx4 v[162:163], v[126:129], off offset:528 sc0 sc1

; __device__ __forceinline__ unsigned cvt_pk_bf16(float lo, float hi) { unsigned r; asm volatile("v_cvt_pk_bf16_f32 %0, %1, %2" : "=v"(r) : "v"(lo), "v"(hi)); return r; }
; __device__ __forceinline__ float fast_sigmoid(float x) { return __builtin_amdgcn_rcpf(1.0f + __builtin_amdgcn_exp2f(-1.44269504089f * x)); }
;     __device__ __forceinline__ void operator()(const f32x4 (&acc)[2][2][4][2], const Unit& u, int wr, int wc, int fr_, int fq_) const {
;     ...
;             for (int m = 0; m < 4; ++m) { const size_t ro = (size_t)(row0 + ai * HALF + m * 16) * 2048 + col0;
; #pragma unroll
;                 for (int bj = 0; bj < 2; ++bj) { f32x4 v0 = acc[ai][bj][m][0], v1 = acc[ai][bj][m][1];
;                     if (mode < 2) { v0 += *(const f32x4*)(bp + col0 + bj * HALF); v1 += *(const f32x4*)(bp + col0 + bj * HALF + 4); }
;                     if (mode == 0) {
; #pragma unroll
;                         for (int j = 0; j < 4; ++j) { const float x0 = -v0[j]; const float s0 = fmaxf(x0, 0.f) + __logf(1.0f + __expf(-fabsf(x0))); v0[j] = __expf(-__expf(-s0 - 0.5f));
;                             const float x1 = -v1[j]; const float s1 = fmaxf(x1, 0.f) + __logf(1.0f + __expf(-fabsf(x1))); v1[j] = __expf(-__expf(-s1 - 0.5f)); } }
;                     else if (mode == 1) {
; #pragma unroll
;                         for (int j = 0; j < 4; ++j) { v0[j] = fast_sigmoid(v0[j]); v1[j] = fast_sigmoid(v1[j]); } }
;                     if (mode == 0) { *(f32x4*)(base + ro + bj * HALF) = v0; *(f32x4*)(base + ro + bj * HALF + 4) = v1; }
;                     else { u32x4 w; w.x = cvt_pk_bf16(v0[0], v0[1]); w.y = cvt_pk_bf16(v0[2], v0[3]); w.z = cvt_pk_bf16(v1[0], v1[1]); w.w = cvt_pk_bf16(v1[2], v1[3]); *(u32x4*)(baseh + ro + bj * HALF) = w; } }
.LBB0_1629:
	v_or_b32_e32 v106, 16, v158
	v_ashrrev_i32_e32 v107, 31, v106
	v_lshlrev_b64 v[106:107], 11, v[106:107]
	v_lshl_add_u64 v[106:107], v[106:107], 0, v[156:157]
	v_lshlrev_b64 v[106:107], 1, v[106:107]
	v_lshl_add_u64 v[122:123], s[90:91], 0, v[106:107]
	s_and_b64 vcc, exec, s[6:7]
	s_mov_b64 s[10:11], -1
	s_cbranch_vccnz .LBB0_1639
	v_cvt_pk_bf16_f32 v108, v114, v115
	v_cvt_pk_bf16_f32 v109, v116, v117
	v_cvt_pk_bf16_f32 v110, v118, v119
	v_cvt_pk_bf16_f32 v111, v120, v121
	global_store_dwordx4 v[122:123], v[108:111], off sc0 sc1
	v_lshl_add_u64 v[124:125], v[122:123], 0, v[106:107]
	s_cbranch_execz .LBB0_1640

; __device__ __forceinline__ unsigned cvt_pk_bf16(float lo, float hi) { unsigned r; asm volatile("v_cvt_pk_bf16_f32 %0, %1, %2" : "=v"(r) : "v"(lo), "v"(hi)); return r; }
;     __device__ __forceinline__ void operator()(const f32x4 (&acc)[2][2][4][2], const Unit& u, int wr, int wc, int fr_, int fq_) const {
;     ...
;                     else { u32x4 w; w.x = cvt_pk_bf16(v0[0], v0[1]); w.y = cvt_pk_bf16(v0[2], v0[3]); w.z = cvt_pk_bf16(v1[0], v1[1]); w.w = cvt_pk_bf16(v1[2], v1[3]); *(u32x4*)(baseh + ro + bj * HALF) = w; } }
.LBB0_1638:
	v_cvt_pk_bf16_f32 v98, v106, v107
	v_cvt_pk_bf16_f32 v99, v108, v109
	v_cvt_pk_bf16_f32 v100, v110, v111
	v_cvt_pk_bf16_f32 v101, v112, v113
	global_store_dwordx4 v[122:123], v[98:101], off offset:256 sc0 sc1
	s_cbranch_execz .LBB0_1644
	s_branch .LBB0_1645

;     __device__ __forceinline__ void operator()(const f32x4 (&acc)[2][2][4][2], const Unit& u, int wr, int wc, int fr_, int fq_) const {
;     ...
;                     if (mode == 0) { *(f32x4*)(base + ro + bj * HALF) = v0; *(f32x4*)(base + ro + bj * HALF + 4) = v1; }
.LBB0_1640:
	global_store_dwordx4 v[124:125], v[114:117], off sc0 sc1
	global_store_dwordx4 v[124:125], v[118:121], off offset:16 sc0 sc1
	s_and_b64 vcc, exec, s[8:9]
	s_cbranch_vccnz .LBB0_1633
	s_branch .LBB0_1632

;     __device__ __forceinline__ void operator()(const f32x4 (&acc)[2][2][4][2], const Unit& u, int wr, int wc, int fr_, int fq_) const {
;     ...
;                     if (mode == 0) { *(f32x4*)(base + ro + bj * HALF) = v0; *(f32x4*)(base + ro + bj * HALF + 4) = v1; }
.LBB0_1644:
	global_store_dwordx4 v[124:125], v[106:109], off offset:512 sc0 sc1
	global_store_dwordx4 v[124:125], v[110:113], off offset:528 sc0 sc1

; __device__ __forceinline__ unsigned cvt_pk_bf16(float lo, float hi) { unsigned r; asm volatile("v_cvt_pk_bf16_f32 %0, %1, %2" : "=v"(r) : "v"(lo), "v"(hi)); return r; }
; __device__ __forceinline__ float fast_sigmoid(float x) { return __builtin_amdgcn_rcpf(1.0f + __builtin_amdgcn_exp2f(-1.44269504089f * x)); }
;     __device__ __forceinline__ void operator()(const f32x4 (&acc)[2][2][4][2], const Unit& u, int wr, int wc, int fr_, int fq_) const {
;     ...
;             for (int m = 0; m < 4; ++m) { const size_t ro = (size_t)(row0 + ai * HALF + m * 16) * 2048 + col0;
; #pragma unroll
;                 for (int bj = 0; bj < 2; ++bj) { f32x4 v0 = acc[ai][bj][m][0], v1 = acc[ai][bj][m][1];
;                     if (mode < 2) { v0 += *(const f32x4*)(bp + col0 + bj * HALF); v1 += *(const f32x4*)(bp + col0 + bj * HALF + 4); }
;                     if (mode == 0) {
; #pragma unroll
;                         for (int j = 0; j < 4; ++j) { const float x0 = -v0[j]; const float s0 = fmaxf(x0, 0.f) + __logf(1.0f + __expf(-fabsf(x0))); v0[j] = __expf(-__expf(-s0 - 0.5f));
;                             const float x1 = -v1[j]; const float s1 = fmaxf(x1, 0.f) + __logf(1.0f + __expf(-fabsf(x1))); v1[j] = __expf(-__expf(-s1 - 0.5f)); } }
;                     else if (mode == 1) {
; #pragma unroll
;                         for (int j = 0; j < 4; ++j) { v0[j] = fast_sigmoid(v0[j]); v1[j] = fast_sigmoid(v1[j]); } }
;                     if (mode == 0) { *(f32x4*)(base + ro + bj * HALF) = v0; *(f32x4*)(base + ro + bj * HALF + 4) = v1; }
;                     else { u32x4 w; w.x = cvt_pk_bf16(v0[0], v0[1]); w.y = cvt_pk_bf16(v0[2], v0[3]); w.z = cvt_pk_bf16(v1[0], v1[1]); w.w = cvt_pk_bf16(v1[2], v1[3]); *(u32x4*)(baseh + ro + bj * HALF) = w; } }
.LBB0_1653:
	v_or_b32_e32 v90, 32, v158
	v_ashrrev_i32_e32 v91, 31, v90
	v_lshlrev_b64 v[90:91], 11, v[90:91]
	v_lshl_add_u64 v[90:91], v[90:91], 0, v[156:157]
	v_lshlrev_b64 v[90:91], 1, v[90:91]
	v_lshl_add_u64 v[106:107], s[90:91], 0, v[90:91]
	s_and_b64 vcc, exec, s[6:7]
	s_mov_b64 s[10:11], -1
	s_cbranch_vccnz .LBB0_1663
	v_cvt_pk_bf16_f32 v92, v98, v99
	v_cvt_pk_bf16_f32 v93, v100, v101
	v_cvt_pk_bf16_f32 v94, v102, v103
	v_cvt_pk_bf16_f32 v95, v104, v105
	global_store_dwordx4 v[106:107], v[92:95], off sc0 sc1
	v_lshl_add_u64 v[108:109], v[106:107], 0, v[90:91]
	s_cbranch_execz .LBB0_1664

; __device__ __forceinline__ unsigned cvt_pk_bf16(float lo, float hi) { unsigned r; asm volatile("v_cvt_pk_bf16_f32 %0, %1, %2" : "=v"(r) : "v"(lo), "v"(hi)); return r; }
;     __device__ __forceinline__ void operator()(const f32x4 (&acc)[2][2][4][2], const Unit& u, int wr, int wc, int fr_, int fq_) const {
;     ...
;                     else { u32x4 w; w.x = cvt_pk_bf16(v0[0], v0[1]); w.y = cvt_pk_bf16(v0[2], v0[3]); w.z = cvt_pk_bf16(v1[0], v1[1]); w.w = cvt_pk_bf16(v1[2], v1[3]); *(u32x4*)(baseh + ro + bj * HALF) = w; } }
.LBB0_1662:
	v_cvt_pk_bf16_f32 v82, v90, v91
	v_cvt_pk_bf16_f32 v83, v92, v93
	v_cvt_pk_bf16_f32 v84, v94, v95
	v_cvt_pk_bf16_f32 v85, v96, v97
	global_store_dwordx4 v[106:107], v[82:85], off offset:256 sc0 sc1
	s_cbranch_execz .LBB0_1668
	s_branch .LBB0_1669

;     __device__ __forceinline__ void operator()(const f32x4 (&acc)[2][2][4][2], const Unit& u, int wr, int wc, int fr_, int fq_) const {
;     ...
;                     if (mode == 0) { *(f32x4*)(base + ro + bj * HALF) = v0; *(f32x4*)(base + ro + bj * HALF + 4) = v1; }
.LBB0_1664:
	global_store_dwordx4 v[108:109], v[98:101], off sc0 sc1
	global_store_dwordx4 v[108:109], v[102:105], off offset:16 sc0 sc1
	s_and_b64 vcc, exec, s[8:9]
	s_cbranch_vccnz .LBB0_1657
	s_branch .LBB0_1656

;     __device__ __forceinline__ void operator()(const f32x4 (&acc)[2][2][4][2], const Unit& u, int wr, int wc, int fr_, int fq_) const {
;     ...
;                     if (mode == 0) { *(f32x4*)(base + ro + bj * HALF) = v0; *(f32x4*)(base + ro + bj * HALF + 4) = v1; }
.LBB0_1668:
	global_store_dwordx4 v[108:109], v[90:93], off offset:512 sc0 sc1
	global_store_dwordx4 v[108:109], v[94:97], off offset:528 sc0 sc1

; __device__ __forceinline__ unsigned cvt_pk_bf16(float lo, float hi) { unsigned r; asm volatile("v_cvt_pk_bf16_f32 %0, %1, %2" : "=v"(r) : "v"(lo), "v"(hi)); return r; }
; __device__ __forceinline__ float fast_sigmoid(float x) { return __builtin_amdgcn_rcpf(1.0f + __builtin_amdgcn_exp2f(-1.44269504089f * x)); }
;     __device__ __forceinline__ void operator()(const f32x4 (&acc)[2][2][4][2], const Unit& u, int wr, int wc, int fr_, int fq_) const {
;     ...
;             for (int m = 0; m < 4; ++m) { const size_t ro = (size_t)(row0 + ai * HALF + m * 16) * 2048 + col0;
; #pragma unroll
;                 for (int bj = 0; bj < 2; ++bj) { f32x4 v0 = acc[ai][bj][m][0], v1 = acc[ai][bj][m][1];
;                     if (mode < 2) { v0 += *(const f32x4*)(bp + col0 + bj * HALF); v1 += *(const f32x4*)(bp + col0 + bj * HALF + 4); }
;                     if (mode == 0) {
; #pragma unroll
;                         for (int j = 0; j < 4; ++j) { const float x0 = -v0[j]; const float s0 = fmaxf(x0, 0.f) + __logf(1.0f + __expf(-fabsf(x0))); v0[j] = __expf(-__expf(-s0 - 0.5f));
;                             const float x1 = -v1[j]; const float s1 = fmaxf(x1, 0.f) + __logf(1.0f + __expf(-fabsf(x1))); v1[j] = __expf(-__expf(-s1 - 0.5f)); } }
;                     else if (mode == 1) {
; #pragma unroll
;                         for (int j = 0; j < 4; ++j) { v0[j] = fast_sigmoid(v0[j]); v1[j] = fast_sigmoid(v1[j]); } }
;                     if (mode == 0) { *(f32x4*)(base + ro + bj * HALF) = v0; *(f32x4*)(base + ro + bj * HALF + 4) = v1; }
;                     else { u32x4 w; w.x = cvt_pk_bf16(v0[0], v0[1]); w.y = cvt_pk_bf16(v0[2], v0[3]); w.z = cvt_pk_bf16(v1[0], v1[1]); w.w = cvt_pk_bf16(v1[2], v1[3]); *(u32x4*)(baseh + ro + bj * HALF) = w; } }
.LBB0_1677:
	v_or_b32_e32 v74, 48, v158
	v_ashrrev_i32_e32 v75, 31, v74
	v_lshlrev_b64 v[74:75], 11, v[74:75]
	v_lshl_add_u64 v[74:75], v[74:75], 0, v[156:157]
	v_lshlrev_b64 v[74:75], 1, v[74:75]
	v_lshl_add_u64 v[90:91], s[90:91], 0, v[74:75]
	s_and_b64 vcc, exec, s[6:7]
	s_mov_b64 s[10:11], -1
	s_cbranch_vccnz .LBB0_1687
	v_cvt_pk_bf16_f32 v76, v82, v83
	v_cvt_pk_bf16_f32 v77, v84, v85
	v_cvt_pk_bf16_f32 v78, v86, v87
	v_cvt_pk_bf16_f32 v79, v88, v89
	global_store_dwordx4 v[90:91], v[76:79], off sc0 sc1
	v_lshl_add_u64 v[92:93], v[90:91], 0, v[74:75]
	s_cbranch_execz .LBB0_1688

; __device__ __forceinline__ unsigned cvt_pk_bf16(float lo, float hi) { unsigned r; asm volatile("v_cvt_pk_bf16_f32 %0, %1, %2" : "=v"(r) : "v"(lo), "v"(hi)); return r; }
;     __device__ __forceinline__ void operator()(const f32x4 (&acc)[2][2][4][2], const Unit& u, int wr, int wc, int fr_, int fq_) const {
;     ...
;                     else { u32x4 w; w.x = cvt_pk_bf16(v0[0], v0[1]); w.y = cvt_pk_bf16(v0[2], v0[3]); w.z = cvt_pk_bf16(v1[0], v1[1]); w.w = cvt_pk_bf16(v1[2], v1[3]); *(u32x4*)(baseh + ro + bj * HALF) = w; } }
.LBB0_1686:
	v_cvt_pk_bf16_f32 v66, v74, v75
	v_cvt_pk_bf16_f32 v67, v76, v77
	v_cvt_pk_bf16_f32 v68, v78, v79
	v_cvt_pk_bf16_f32 v69, v80, v81
	global_store_dwordx4 v[90:91], v[66:69], off offset:256 sc0 sc1
	s_cbranch_execz .LBB0_1692
	s_branch .LBB0_1693

;     __device__ __forceinline__ void operator()(const f32x4 (&acc)[2][2][4][2], const Unit& u, int wr, int wc, int fr_, int fq_) const {
;     ...
;                     if (mode == 0) { *(f32x4*)(base + ro + bj * HALF) = v0; *(f32x4*)(base + ro + bj * HALF + 4) = v1; }
.LBB0_1688:
	global_store_dwordx4 v[92:93], v[82:85], off sc0 sc1
	global_store_dwordx4 v[92:93], v[86:89], off offset:16 sc0 sc1
	s_and_b64 vcc, exec, s[8:9]
	s_cbranch_vccnz .LBB0_1681
	s_branch .LBB0_1680

;     __device__ __forceinline__ void operator()(const f32x4 (&acc)[2][2][4][2], const Unit& u, int wr, int wc, int fr_, int fq_) const {
;     ...
;                     if (mode == 0) { *(f32x4*)(base + ro + bj * HALF) = v0; *(f32x4*)(base + ro + bj * HALF + 4) = v1; }
.LBB0_1692:
	global_store_dwordx4 v[92:93], v[74:77], off offset:512 sc0 sc1
	global_store_dwordx4 v[92:93], v[78:81], off offset:528 sc0 sc1

; __device__ __forceinline__ unsigned cvt_pk_bf16(float lo, float hi) { unsigned r; asm volatile("v_cvt_pk_bf16_f32 %0, %1, %2" : "=v"(r) : "v"(lo), "v"(hi)); return r; }
; __device__ __forceinline__ float fast_sigmoid(float x) { return __builtin_amdgcn_rcpf(1.0f + __builtin_amdgcn_exp2f(-1.44269504089f * x)); }
;     __device__ __forceinline__ void operator()(const f32x4 (&acc)[2][2][4][2], const Unit& u, int wr, int wc, int fr_, int fq_) const {
;     ...
;             for (int m = 0; m < 4; ++m) { const size_t ro = (size_t)(row0 + ai * HALF + m * 16) * 2048 + col0;
; #pragma unroll
;                 for (int bj = 0; bj < 2; ++bj) { f32x4 v0 = acc[ai][bj][m][0], v1 = acc[ai][bj][m][1];
;                     if (mode < 2) { v0 += *(const f32x4*)(bp + col0 + bj * HALF); v1 += *(const f32x4*)(bp + col0 + bj * HALF + 4); }
;                     if (mode == 0) {
; #pragma unroll
;                         for (int j = 0; j < 4; ++j) { const float x0 = -v0[j]; const float s0 = fmaxf(x0, 0.f) + __logf(1.0f + __expf(-fabsf(x0))); v0[j] = __expf(-__expf(-s0 - 0.5f));
;                             const float x1 = -v1[j]; const float s1 = fmaxf(x1, 0.f) + __logf(1.0f + __expf(-fabsf(x1))); v1[j] = __expf(-__expf(-s1 - 0.5f)); } }
;                     else if (mode == 1) {
; #pragma unroll
;                         for (int j = 0; j < 4; ++j) { v0[j] = fast_sigmoid(v0[j]); v1[j] = fast_sigmoid(v1[j]); } }
;                     if (mode == 0) { *(f32x4*)(base + ro + bj * HALF) = v0; *(f32x4*)(base + ro + bj * HALF + 4) = v1; }
;                     else { u32x4 w; w.x = cvt_pk_bf16(v0[0], v0[1]); w.y = cvt_pk_bf16(v0[2], v0[3]); w.z = cvt_pk_bf16(v1[0], v1[1]); w.w = cvt_pk_bf16(v1[2], v1[3]); *(u32x4*)(baseh + ro + bj * HALF) = w; } }
.LBB0_1701:
	v_lshlrev_b64 v[58:59], 11, v[158:159]
	v_lshl_add_u64 v[58:59], v[58:59], 0, v[156:157]
	v_lshl_add_u64 v[58:59], v[58:59], 1, v[252:253]
	v_lshl_add_u64 v[74:75], s[90:91], 0, v[58:59]
	s_and_b64 vcc, exec, s[6:7]
	s_mov_b64 s[10:11], -1
	s_cbranch_vccnz .LBB0_1711
	v_cvt_pk_bf16_f32 v60, v66, v67
	v_cvt_pk_bf16_f32 v61, v68, v69
	v_cvt_pk_bf16_f32 v62, v70, v71
	v_cvt_pk_bf16_f32 v63, v72, v73
	global_store_dwordx4 v[74:75], v[60:63], off sc0 sc1
	v_lshl_add_u64 v[76:77], v[74:75], 0, v[58:59]
	s_cbranch_execz .LBB0_1712

; __device__ __forceinline__ unsigned cvt_pk_bf16(float lo, float hi) { unsigned r; asm volatile("v_cvt_pk_bf16_f32 %0, %1, %2" : "=v"(r) : "v"(lo), "v"(hi)); return r; }
;     __device__ __forceinline__ void operator()(const f32x4 (&acc)[2][2][4][2], const Unit& u, int wr, int wc, int fr_, int fq_) const {
;     ...
;                     else { u32x4 w; w.x = cvt_pk_bf16(v0[0], v0[1]); w.y = cvt_pk_bf16(v0[2], v0[3]); w.z = cvt_pk_bf16(v1[0], v1[1]); w.w = cvt_pk_bf16(v1[2], v1[3]); *(u32x4*)(baseh + ro + bj * HALF) = w; } }
.LBB0_1710:
	v_cvt_pk_bf16_f32 v50, v58, v59
	v_cvt_pk_bf16_f32 v51, v60, v61
	v_cvt_pk_bf16_f32 v52, v62, v63
	v_cvt_pk_bf16_f32 v53, v64, v65
	global_store_dwordx4 v[74:75], v[50:53], off offset:256 sc0 sc1
	s_cbranch_execz .LBB0_1716
	s_branch .LBB0_1717

;     __device__ __forceinline__ void operator()(const f32x4 (&acc)[2][2][4][2], const Unit& u, int wr, int wc, int fr_, int fq_) const {
;     ...
;                     if (mode == 0) { *(f32x4*)(base + ro + bj * HALF) = v0; *(f32x4*)(base + ro + bj * HALF + 4) = v1; }
.LBB0_1712:
	global_store_dwordx4 v[76:77], v[66:69], off sc0 sc1
	global_store_dwordx4 v[76:77], v[70:73], off offset:16 sc0 sc1
	s_and_b64 vcc, exec, s[8:9]
	s_cbranch_vccnz .LBB0_1705
	s_branch .LBB0_1704

;     __device__ __forceinline__ void operator()(const f32x4 (&acc)[2][2][4][2], const Unit& u, int wr, int wc, int fr_, int fq_) const {
;     ...
;                     if (mode == 0) { *(f32x4*)(base + ro + bj * HALF) = v0; *(f32x4*)(base + ro + bj * HALF + 4) = v1; }
.LBB0_1716:
	global_store_dwordx4 v[76:77], v[58:61], off offset:512 sc0 sc1
	global_store_dwordx4 v[76:77], v[62:65], off offset:528 sc0 sc1

; __device__ __forceinline__ unsigned cvt_pk_bf16(float lo, float hi) { unsigned r; asm volatile("v_cvt_pk_bf16_f32 %0, %1, %2" : "=v"(r) : "v"(lo), "v"(hi)); return r; }
; __device__ __forceinline__ float fast_sigmoid(float x) { return __builtin_amdgcn_rcpf(1.0f + __builtin_amdgcn_exp2f(-1.44269504089f * x)); }
;     __device__ __forceinline__ void operator()(const f32x4 (&acc)[2][2][4][2], const Unit& u, int wr, int wc, int fr_, int fq_) const {
;     ...
;             for (int m = 0; m < 4; ++m) { const size_t ro = (size_t)(row0 + ai * HALF + m * 16) * 2048 + col0;
; #pragma unroll
;                 for (int bj = 0; bj < 2; ++bj) { f32x4 v0 = acc[ai][bj][m][0], v1 = acc[ai][bj][m][1];
;                     if (mode < 2) { v0 += *(const f32x4*)(bp + col0 + bj * HALF); v1 += *(const f32x4*)(bp + col0 + bj * HALF + 4); }
;                     if (mode == 0) {
; #pragma unroll
;                         for (int j = 0; j < 4; ++j) { const float x0 = -v0[j]; const float s0 = fmaxf(x0, 0.f) + __logf(1.0f + __expf(-fabsf(x0))); v0[j] = __expf(-__expf(-s0 - 0.5f));
;                             const float x1 = -v1[j]; const float s1 = fmaxf(x1, 0.f) + __logf(1.0f + __expf(-fabsf(x1))); v1[j] = __expf(-__expf(-s1 - 0.5f)); } }
;                     else if (mode == 1) {
; #pragma unroll
;                         for (int j = 0; j < 4; ++j) { v0[j] = fast_sigmoid(v0[j]); v1[j] = fast_sigmoid(v1[j]); } }
;                     if (mode == 0) { *(f32x4*)(base + ro + bj * HALF) = v0; *(f32x4*)(base + ro + bj * HALF + 4) = v1; }
;                     else { u32x4 w; w.x = cvt_pk_bf16(v0[0], v0[1]); w.y = cvt_pk_bf16(v0[2], v0[3]); w.z = cvt_pk_bf16(v1[0], v1[1]); w.w = cvt_pk_bf16(v1[2], v1[3]); *(u32x4*)(baseh + ro + bj * HALF) = w; } }
.LBB0_1725:
	v_lshlrev_b64 v[42:43], 11, v[158:159]
	v_lshl_add_u64 v[42:43], v[42:43], 0, v[156:157]
	v_mov_b64_e32 v[44:45], 0x90000
	v_lshl_add_u64 v[42:43], v[42:43], 1, v[44:45]
	v_lshl_add_u64 v[58:59], s[90:91], 0, v[42:43]
	s_and_b64 vcc, exec, s[6:7]
	s_mov_b64 s[10:11], -1
	s_cbranch_vccnz .LBB0_1735
	v_cvt_pk_bf16_f32 v44, v50, v51
	v_cvt_pk_bf16_f32 v45, v52, v53
	v_cvt_pk_bf16_f32 v46, v54, v55
	v_cvt_pk_bf16_f32 v47, v56, v57
	global_store_dwordx4 v[58:59], v[44:47], off sc0 sc1
	v_lshl_add_u64 v[60:61], v[58:59], 0, v[42:43]
	s_cbranch_execz .LBB0_1736

; __device__ __forceinline__ unsigned cvt_pk_bf16(float lo, float hi) { unsigned r; asm volatile("v_cvt_pk_bf16_f32 %0, %1, %2" : "=v"(r) : "v"(lo), "v"(hi)); return r; }
;     __device__ __forceinline__ void operator()(const f32x4 (&acc)[2][2][4][2], const Unit& u, int wr, int wc, int fr_, int fq_) const {
;     ...
;                     else { u32x4 w; w.x = cvt_pk_bf16(v0[0], v0[1]); w.y = cvt_pk_bf16(v0[2], v0[3]); w.z = cvt_pk_bf16(v1[0], v1[1]); w.w = cvt_pk_bf16(v1[2], v1[3]); *(u32x4*)(baseh + ro + bj * HALF) = w; } }
.LBB0_1734:
	v_cvt_pk_bf16_f32 v34, v42, v43
	v_cvt_pk_bf16_f32 v35, v44, v45
	v_cvt_pk_bf16_f32 v36, v46, v47
	v_cvt_pk_bf16_f32 v37, v48, v49
	global_store_dwordx4 v[58:59], v[34:37], off offset:256 sc0 sc1
	s_cbranch_execz .LBB0_1740
	s_branch .LBB0_1741

;     __device__ __forceinline__ void operator()(const f32x4 (&acc)[2][2][4][2], const Unit& u, int wr, int wc, int fr_, int fq_) const {
;     ...
;                     if (mode == 0) { *(f32x4*)(base + ro + bj * HALF) = v0; *(f32x4*)(base + ro + bj * HALF + 4) = v1; }
.LBB0_1736:
	global_store_dwordx4 v[60:61], v[50:53], off sc0 sc1
	global_store_dwordx4 v[60:61], v[54:57], off offset:16 sc0 sc1
	s_and_b64 vcc, exec, s[8:9]
	s_cbranch_vccnz .LBB0_1729
	s_branch .LBB0_1728

;     __device__ __forceinline__ void operator()(const f32x4 (&acc)[2][2][4][2], const Unit& u, int wr, int wc, int fr_, int fq_) const {
;     ...
;                     if (mode == 0) { *(f32x4*)(base + ro + bj * HALF) = v0; *(f32x4*)(base + ro + bj * HALF + 4) = v1; }
.LBB0_1740:
	global_store_dwordx4 v[60:61], v[42:45], off offset:512 sc0 sc1
	global_store_dwordx4 v[60:61], v[46:49], off offset:528 sc0 sc1

; __device__ __forceinline__ unsigned cvt_pk_bf16(float lo, float hi) { unsigned r; asm volatile("v_cvt_pk_bf16_f32 %0, %1, %2" : "=v"(r) : "v"(lo), "v"(hi)); return r; }
; __device__ __forceinline__ float fast_sigmoid(float x) { return __builtin_amdgcn_rcpf(1.0f + __builtin_amdgcn_exp2f(-1.44269504089f * x)); }
;     __device__ __forceinline__ void operator()(const f32x4 (&acc)[2][2][4][2], const Unit& u, int wr, int wc, int fr_, int fq_) const {
;     ...
;             for (int m = 0; m < 4; ++m) { const size_t ro = (size_t)(row0 + ai * HALF + m * 16) * 2048 + col0;
; #pragma unroll
;                 for (int bj = 0; bj < 2; ++bj) { f32x4 v0 = acc[ai][bj][m][0], v1 = acc[ai][bj][m][1];
;                     if (mode < 2) { v0 += *(const f32x4*)(bp + col0 + bj * HALF); v1 += *(const f32x4*)(bp + col0 + bj * HALF + 4); }
;                     if (mode == 0) {
; #pragma unroll
;                         for (int j = 0; j < 4; ++j) { const float x0 = -v0[j]; const float s0 = fmaxf(x0, 0.f) + __logf(1.0f + __expf(-fabsf(x0))); v0[j] = __expf(-__expf(-s0 - 0.5f));
;                             const float x1 = -v1[j]; const float s1 = fmaxf(x1, 0.f) + __logf(1.0f + __expf(-fabsf(x1))); v1[j] = __expf(-__expf(-s1 - 0.5f)); } }
;                     else if (mode == 1) {
; #pragma unroll
;                         for (int j = 0; j < 4; ++j) { v0[j] = fast_sigmoid(v0[j]); v1[j] = fast_sigmoid(v1[j]); } }
;                     if (mode == 0) { *(f32x4*)(base + ro + bj * HALF) = v0; *(f32x4*)(base + ro + bj * HALF + 4) = v1; }
;                     else { u32x4 w; w.x = cvt_pk_bf16(v0[0], v0[1]); w.y = cvt_pk_bf16(v0[2], v0[3]); w.z = cvt_pk_bf16(v1[0], v1[1]); w.w = cvt_pk_bf16(v1[2], v1[3]); *(u32x4*)(baseh + ro + bj * HALF) = w; } }
.LBB0_1749:
	v_lshlrev_b64 v[26:27], 11, v[158:159]
	v_lshl_add_u64 v[26:27], v[26:27], 0, v[156:157]
	v_lshl_add_u64 v[26:27], v[26:27], 1, v[150:151]
	v_lshl_add_u64 v[42:43], s[90:91], 0, v[26:27]
	s_and_b64 vcc, exec, s[6:7]
	s_mov_b64 s[10:11], -1
	s_cbranch_vccnz .LBB0_1759
	v_cvt_pk_bf16_f32 v28, v34, v35
	v_cvt_pk_bf16_f32 v29, v36, v37
	v_cvt_pk_bf16_f32 v30, v38, v39
	v_cvt_pk_bf16_f32 v31, v40, v41
	global_store_dwordx4 v[42:43], v[28:31], off sc0 sc1
	v_lshl_add_u64 v[44:45], v[42:43], 0, v[26:27]
	s_cbranch_execz .LBB0_1760

; __device__ __forceinline__ unsigned cvt_pk_bf16(float lo, float hi) { unsigned r; asm volatile("v_cvt_pk_bf16_f32 %0, %1, %2" : "=v"(r) : "v"(lo), "v"(hi)); return r; }
;     __device__ __forceinline__ void operator()(const f32x4 (&acc)[2][2][4][2], const Unit& u, int wr, int wc, int fr_, int fq_) const {
;     ...
;                     else { u32x4 w; w.x = cvt_pk_bf16(v0[0], v0[1]); w.y = cvt_pk_bf16(v0[2], v0[3]); w.z = cvt_pk_bf16(v1[0], v1[1]); w.w = cvt_pk_bf16(v1[2], v1[3]); *(u32x4*)(baseh + ro + bj * HALF) = w; } }
.LBB0_1758:
	v_cvt_pk_bf16_f32 v18, v26, v27
	v_cvt_pk_bf16_f32 v19, v28, v29
	v_cvt_pk_bf16_f32 v20, v30, v31
	v_cvt_pk_bf16_f32 v21, v32, v33
	global_store_dwordx4 v[42:43], v[18:21], off offset:256 sc0 sc1
	s_cbranch_execz .LBB0_1764
	s_branch .LBB0_1765

;     __device__ __forceinline__ void operator()(const f32x4 (&acc)[2][2][4][2], const Unit& u, int wr, int wc, int fr_, int fq_) const {
;     ...
;                     if (mode == 0) { *(f32x4*)(base + ro + bj * HALF) = v0; *(f32x4*)(base + ro + bj * HALF + 4) = v1; }
.LBB0_1760:
	global_store_dwordx4 v[44:45], v[34:37], off sc0 sc1
	global_store_dwordx4 v[44:45], v[38:41], off offset:16 sc0 sc1
	s_and_b64 vcc, exec, s[8:9]
	s_cbranch_vccnz .LBB0_1753
	s_branch .LBB0_1752

;     __device__ __forceinline__ void operator()(const f32x4 (&acc)[2][2][4][2], const Unit& u, int wr, int wc, int fr_, int fq_) const {
;     ...
;                     if (mode == 0) { *(f32x4*)(base + ro + bj * HALF) = v0; *(f32x4*)(base + ro + bj * HALF + 4) = v1; }
.LBB0_1764:
	global_store_dwordx4 v[44:45], v[26:29], off offset:512 sc0 sc1
	global_store_dwordx4 v[44:45], v[30:33], off offset:528 sc0 sc1

; __device__ __forceinline__ unsigned cvt_pk_bf16(float lo, float hi) { unsigned r; asm volatile("v_cvt_pk_bf16_f32 %0, %1, %2" : "=v"(r) : "v"(lo), "v"(hi)); return r; }
; __device__ __forceinline__ float fast_sigmoid(float x) { return __builtin_amdgcn_rcpf(1.0f + __builtin_amdgcn_exp2f(-1.44269504089f * x)); }
;     __device__ __forceinline__ void operator()(const f32x4 (&acc)[2][2][4][2], const Unit& u, int wr, int wc, int fr_, int fq_) const {
;     ...
;             for (int m = 0; m < 4; ++m) { const size_t ro = (size_t)(row0 + ai * HALF + m * 16) * 2048 + col0;
; #pragma unroll
;                 for (int bj = 0; bj < 2; ++bj) { f32x4 v0 = acc[ai][bj][m][0], v1 = acc[ai][bj][m][1];
;                     if (mode < 2) { v0 += *(const f32x4*)(bp + col0 + bj * HALF); v1 += *(const f32x4*)(bp + col0 + bj * HALF + 4); }
;                     if (mode == 0) {
; #pragma unroll
;                         for (int j = 0; j < 4; ++j) { const float x0 = -v0[j]; const float s0 = fmaxf(x0, 0.f) + __logf(1.0f + __expf(-fabsf(x0))); v0[j] = __expf(-__expf(-s0 - 0.5f));
;                             const float x1 = -v1[j]; const float s1 = fmaxf(x1, 0.f) + __logf(1.0f + __expf(-fabsf(x1))); v1[j] = __expf(-__expf(-s1 - 0.5f)); } }
;                     else if (mode == 1) {
; #pragma unroll
;                         for (int j = 0; j < 4; ++j) { v0[j] = fast_sigmoid(v0[j]); v1[j] = fast_sigmoid(v1[j]); } }
;                     if (mode == 0) { *(f32x4*)(base + ro + bj * HALF) = v0; *(f32x4*)(base + ro + bj * HALF + 4) = v1; }
;                     else { u32x4 w; w.x = cvt_pk_bf16(v0[0], v0[1]); w.y = cvt_pk_bf16(v0[2], v0[3]); w.z = cvt_pk_bf16(v1[0], v1[1]); w.w = cvt_pk_bf16(v1[2], v1[3]); *(u32x4*)(baseh + ro + bj * HALF) = w; } }
.LBB0_1773:
	v_lshlrev_b64 v[10:11], 11, v[158:159]
	v_lshl_add_u64 v[10:11], v[10:11], 0, v[156:157]
	v_lshl_add_u64 v[10:11], v[10:11], 1, v[152:153]
	v_lshl_add_u64 v[26:27], s[90:91], 0, v[10:11]
	s_and_b64 vcc, exec, s[6:7]
	s_mov_b64 s[10:11], -1
	s_cbranch_vccnz .LBB0_1783
	v_cvt_pk_bf16_f32 v12, v18, v19
	v_cvt_pk_bf16_f32 v13, v20, v21
	v_cvt_pk_bf16_f32 v14, v22, v23
	v_cvt_pk_bf16_f32 v15, v24, v25
	global_store_dwordx4 v[26:27], v[12:15], off sc0 sc1
	v_lshl_add_u64 v[28:29], v[26:27], 0, v[10:11]
	s_cbranch_execz .LBB0_1784

; __device__ __forceinline__ unsigned cvt_pk_bf16(float lo, float hi) { unsigned r; asm volatile("v_cvt_pk_bf16_f32 %0, %1, %2" : "=v"(r) : "v"(lo), "v"(hi)); return r; }
;     __device__ __forceinline__ void operator()(const f32x4 (&acc)[2][2][4][2], const Unit& u, int wr, int wc, int fr_, int fq_) const {
;     ...
;                     else { u32x4 w; w.x = cvt_pk_bf16(v0[0], v0[1]); w.y = cvt_pk_bf16(v0[2], v0[3]); w.z = cvt_pk_bf16(v1[0], v1[1]); w.w = cvt_pk_bf16(v1[2], v1[3]); *(u32x4*)(baseh + ro + bj * HALF) = w; } }
.LBB0_1782:
	v_cvt_pk_bf16_f32 v2, v10, v11
	v_cvt_pk_bf16_f32 v3, v12, v13
	v_cvt_pk_bf16_f32 v4, v14, v15
	v_cvt_pk_bf16_f32 v5, v16, v17
	global_store_dwordx4 v[26:27], v[2:5], off offset:256 sc0 sc1
	s_cbranch_execz .LBB0_1788
	s_branch .LBB0_1789

;     __device__ __forceinline__ void operator()(const f32x4 (&acc)[2][2][4][2], const Unit& u, int wr, int wc, int fr_, int fq_) const {
;     ...
;                     if (mode == 0) { *(f32x4*)(base + ro + bj * HALF) = v0; *(f32x4*)(base + ro + bj * HALF + 4) = v1; }
.LBB0_1784:
	global_store_dwordx4 v[28:29], v[18:21], off sc0 sc1
	global_store_dwordx4 v[28:29], v[22:25], off offset:16 sc0 sc1
	s_and_b64 vcc, exec, s[8:9]
	s_cbranch_vccnz .LBB0_1777
	s_branch .LBB0_1776

;     __device__ __forceinline__ void operator()(const f32x4 (&acc)[2][2][4][2], const Unit& u, int wr, int wc, int fr_, int fq_) const {
;     ...
;                     if (mode == 0) { *(f32x4*)(base + ro + bj * HALF) = v0; *(f32x4*)(base + ro + bj * HALF + 4) = v1; }
.LBB0_1788:
	global_store_dwordx4 v[28:29], v[10:13], off offset:512 sc0 sc1
	global_store_dwordx4 v[28:29], v[14:17], off offset:528 sc0 sc1

; __device__ __forceinline__ int fresh_lane() { int l; asm volatile("v_mbcnt_lo_u32_b32 %0, -1, 0\n\tv_mbcnt_hi_u32_b32 %0, -1, %0" : "=v"(l)); return l; }
; __device__ __forceinline__ unsigned cvt_pk_bf16(float lo, float hi) { unsigned r; asm volatile("v_cvt_pk_bf16_f32 %0, %1, %2" : "=v"(r) : "v"(lo), "v"(hi)); return r; }
;     __device__ __forceinline__ void operator()(const f32x4 (&acc)[2][2][4][2], const Unit& u, int wr, int wc, int fr_, int fq_) const {
;         const int l_ = fresh_lane(), fr = l_ & 15, fq = l_ >> 4;
;         const int row0 = u.pm * BM + wr * 64 + fr, col0 = u.pn * BM + wc * 32 + 8 * fq;
; #pragma unroll
;         for (int ai = 0; ai < 2; ++ai)
; #pragma unroll
;             for (int m = 0; m < 4; ++m) { bf16_t* rowp = O + (size_t)(row0 + ai * HALF + m * 16) * ldc + col0;
; #pragma unroll
;                 for (int bj = 0; bj < 2; ++bj) { const f32x4 v0 = acc[ai][bj][m][0], v1 = acc[ai][bj][m][1];
;                     u32x4 w; w.x = cvt_pk_bf16(v0[0], v0[1]); w.y = cvt_pk_bf16(v0[2], v0[3]); w.z = cvt_pk_bf16(v1[0], v1[1]); w.w = cvt_pk_bf16(v1[2], v1[3]);
;                     *(u32x4*)(rowp + bj * HALF) = w; } }
.LBB0_3154:
	s_lshl_b32 s39, s46, 8
	v_mbcnt_lo_u32_b32 v140, -1, 0
	v_mbcnt_hi_u32_b32 v140, -1, v140
	s_add_i32 s39, s39, s62
	v_and_or_b32 v146, v140, 15, s39
	s_lshl_b32 s39, s74, 8
	v_ashrrev_i32_e32 v140, 1, v140
	s_or_b32 s39, s39, s63
	v_and_b32_e32 v140, -8, v140
	v_add_u32_e32 v140, s39, v140
	v_ashrrev_i32_e32 v147, 31, v146
	v_ashrrev_i32_e32 v141, 31, v140
	v_lshlrev_b64 v[148:149], 12, v[146:147]
	v_lshl_add_u64 v[148:149], s[12:13], 0, v[148:149]
	v_lshlrev_b64 v[150:151], 1, v[140:141]
	v_lshl_add_u64 v[140:141], v[148:149], 0, v[150:151]
	v_cvt_pk_bf16_f32 v126, v126, v127
	v_cvt_pk_bf16_f32 v127, v128, v129
	v_cvt_pk_bf16_f32 v128, v122, v123
	v_cvt_pk_bf16_f32 v129, v124, v125
	global_store_dwordx4 v[140:141], v[126:129], off sc0 sc1
	v_cvt_pk_bf16_f32 v114, v114, v115
	v_cvt_pk_bf16_f32 v115, v116, v117
	v_cvt_pk_bf16_f32 v116, v106, v107
	v_or_b32_e32 v106, 16, v146
	v_ashrrev_i32_e32 v107, 31, v106
	v_lshlrev_b64 v[106:107], 12, v[106:107]
	v_lshl_add_u64 v[106:107], s[12:13], 0, v[106:107]
	v_cvt_pk_bf16_f32 v117, v108, v109
	global_store_dwordx4 v[140:141], v[114:117], off offset:256 sc0 sc1
	s_nop 1
	v_lshl_add_u64 v[114:115], v[106:107], 0, v[150:151]
	v_cvt_pk_bf16_f32 v106, v118, v119
	v_cvt_pk_bf16_f32 v107, v120, v121
	v_cvt_pk_bf16_f32 v108, v110, v111
	v_cvt_pk_bf16_f32 v109, v112, v113
	global_store_dwordx4 v[114:115], v[106:109], off sc0 sc1
	v_cvt_pk_bf16_f32 v98, v98, v99
	v_cvt_pk_bf16_f32 v99, v100, v101
	v_cvt_pk_bf16_f32 v100, v90, v91
	v_or_b32_e32 v90, 32, v146
	v_ashrrev_i32_e32 v91, 31, v90
	v_lshlrev_b64 v[90:91], 12, v[90:91]
	v_lshl_add_u64 v[90:91], s[12:13], 0, v[90:91]
	v_cvt_pk_bf16_f32 v101, v92, v93
	global_store_dwordx4 v[114:115], v[98:101], off offset:256 sc0 sc1
	s_nop 1
	v_lshl_add_u64 v[98:99], v[90:91], 0, v[150:151]
	v_cvt_pk_bf16_f32 v90, v102, v103
	v_cvt_pk_bf16_f32 v91, v104, v105
	v_cvt_pk_bf16_f32 v92, v94, v95
	v_cvt_pk_bf16_f32 v93, v96, v97
	global_store_dwordx4 v[98:99], v[90:93], off sc0 sc1
	v_cvt_pk_bf16_f32 v82, v82, v83
	v_cvt_pk_bf16_f32 v83, v84, v85
	v_cvt_pk_bf16_f32 v84, v74, v75
	v_or_b32_e32 v74, 48, v146
	v_ashrrev_i32_e32 v75, 31, v74
	v_lshlrev_b64 v[74:75], 12, v[74:75]
	v_lshl_add_u64 v[74:75], s[12:13], 0, v[74:75]
	v_cvt_pk_bf16_f32 v85, v76, v77
	global_store_dwordx4 v[98:99], v[82:85], off offset:256 sc0 sc1
	s_nop 1
	v_lshl_add_u64 v[82:83], v[74:75], 0, v[150:151]
	v_cvt_pk_bf16_f32 v74, v86, v87
	v_cvt_pk_bf16_f32 v75, v88, v89
	v_cvt_pk_bf16_f32 v76, v78, v79
	v_cvt_pk_bf16_f32 v77, v80, v81
	global_store_dwordx4 v[82:83], v[74:77], off sc0 sc1
	v_cvt_pk_bf16_f32 v70, v70, v71
	v_cvt_pk_bf16_f32 v71, v72, v73
	v_cvt_pk_bf16_f32 v72, v66, v67
	v_cvt_pk_bf16_f32 v73, v68, v69
	global_store_dwordx4 v[82:83], v[70:73], off offset:256 sc0 sc1
	v_cvt_pk_bf16_f32 v62, v62, v63
	v_cvt_pk_bf16_f32 v63, v64, v65
	v_cvt_pk_bf16_f32 v64, v58, v59
	v_add_co_u32_e32 v58, vcc, s66, v140
	v_lshl_add_u64 v[66:67], v[140:141], 0, s[4:5]
	s_nop 0
	v_addc_co_u32_e32 v59, vcc, 0, v141, vcc
	v_cvt_pk_bf16_f32 v65, v60, v61
	global_store_dwordx4 v[58:59], v[62:65], off sc0 sc1
	v_cvt_pk_bf16_f32 v50, v50, v51
	v_cvt_pk_bf16_f32 v51, v52, v53
	v_cvt_pk_bf16_f32 v52, v42, v43
	v_cvt_pk_bf16_f32 v53, v44, v45
	global_store_dwordx4 v[66:67], v[50:53], off offset:256 sc0 sc1
	v_cvt_pk_bf16_f32 v42, v54, v55
	v_cvt_pk_bf16_f32 v43, v56, v57
	v_cvt_pk_bf16_f32 v44, v46, v47
	v_add_co_u32_e32 v46, vcc, s67, v140
	s_nop 0
	v_lshl_add_u64 v[50:51], v[140:141], 0, s[28:29]
	v_addc_co_u32_e32 v47, vcc, 0, v141, vcc
	v_cvt_pk_bf16_f32 v45, v48, v49
	global_store_dwordx4 v[46:47], v[42:45], off sc0 sc1
	v_cvt_pk_bf16_f32 v34, v34, v35
	v_cvt_pk_bf16_f32 v35, v36, v37
	v_cvt_pk_bf16_f32 v36, v26, v27
	v_cvt_pk_bf16_f32 v37, v28, v29
	global_store_dwordx4 v[50:51], v[34:37], off offset:256 sc0 sc1
	v_cvt_pk_bf16_f32 v26, v38, v39
	v_cvt_pk_bf16_f32 v27, v40, v41
	v_cvt_pk_bf16_f32 v28, v30, v31
	v_add_co_u32_e32 v30, vcc, s70, v140
	s_nop 0
	v_lshl_add_u64 v[34:35], v[140:141], 0, s[30:31]
	v_addc_co_u32_e32 v31, vcc, 0, v141, vcc
	v_cvt_pk_bf16_f32 v29, v32, v33
	global_store_dwordx4 v[30:31], v[26:29], off sc0 sc1
	v_cvt_pk_bf16_f32 v18, v18, v19
	v_cvt_pk_bf16_f32 v19, v20, v21
	v_cvt_pk_bf16_f32 v20, v10, v11
	v_cvt_pk_bf16_f32 v21, v12, v13
	global_store_dwordx4 v[34:35], v[18:21], off offset:256 sc0 sc1
	v_cvt_pk_bf16_f32 v10, v22, v23
	v_cvt_pk_bf16_f32 v11, v24, v25
	v_cvt_pk_bf16_f32 v12, v14, v15
	v_add_co_u32_e32 v14, vcc, s71, v140
	s_nop 0
	v_lshl_add_u64 v[18:19], v[140:141], 0, s[36:37]
	v_addc_co_u32_e32 v15, vcc, 0, v141, vcc
	s_andn2_b64 vcc, exec, s[0:1]
	s_mov_b64 s[0:1], -1
	v_cvt_pk_bf16_f32 v13, v16, v17
	global_store_dwordx4 v[14:15], v[10:13], off sc0 sc1
	v_cvt_pk_bf16_f32 v6, v6, v7
	v_cvt_pk_bf16_f32 v7, v8, v9
	v_cvt_pk_bf16_f32 v8, v2, v3
	v_cvt_pk_bf16_f32 v9, v4, v5
	global_store_dwordx4 v[18:19], v[6:9], off offset:256 sc0 sc1
	s_cbranch_vccnz .LBB0_3143
	s_andn2_b64 vcc, exec, s[10:11]
	s_cbranch_vccnz .LBB0_3142
	s_barrier
	s_branch .LBB0_3142
